# P7 fixed conversion share: hand-written 3-deep loop, concurrent items ordered as 2 row blocks x 4 column blocks (longer contiguous fp8 writes)
# speedup vs baseline: 1.0062x; 1.0062x over previous
.LBB0_993:
	s_add_u32 s38, s90, 0x4b100000
	s_addc_u32 s39, s91, 0
	v_readlane_b32 s3, v255, 4
	s_bitcmp0_b32 s3, 0
	s_cbranch_scc1 .LBB0_1024
	s_waitcnt vmcnt(0)
	s_lshl_b32 s0, s3, 6
	s_and_b32 s0, s0, 0xffffff80
	v_readlane_b32 s2, v255, 28
	s_and_b32 s1, s2, 1
	s_lshl_b32 s1, s1, 6
	s_lshr_b32 s2, s2, 1
	s_add_i32 s2, s2, s1
	s_add_i32 s20, s2, s0
	v_mbcnt_lo_u32_b32 v210, -1, 0
	v_mbcnt_hi_u32_b32 v210, -1, v210
	v_lshrrev_b32_e32 v211, 3, v210
	v_and_b32_e32 v210, 7, v210
	v_lshlrev_b32_e32 v208, 17, v211
	v_lshl_or_b32 v208, v210, 4, v208
	v_lshlrev_b32_e32 v209, 13, v210
	v_lshl_or_b32 v209, v211, 4, v209
	s_mov_b32 s16, 0x44000000
	s_add_i32 s1, s20, 0
	s_lshr_b32 s2, s1, 10
	s_and_b32 s4, s1, 0x3ff
	s_lshr_b32 s5, s4, 6
	s_and_b32 s4, s4, 63
	s_lshl_b32 s12, s2, 24
	s_lshl_b32 s13, s5, 20
	s_add_i32 s12, s12, s13
	s_lshl_b32 s13, s4, 7
	s_add_i32 s12, s12, s13
	s_add_u32 s14, s70, s12
	s_addc_u32 s15, s71, 0
	global_load_dwordx4 v[0:3], v208, s[14:15] sc1 nt
	s_add_u32 s18, s14, 0x2000
	s_addc_u32 s19, s15, 0
	global_load_dwordx4 v[4:7], v208, s[18:19] sc1 nt
	s_add_u32 s18, s14, 0x4000
	s_addc_u32 s19, s15, 0
	global_load_dwordx4 v[8:11], v208, s[18:19] sc1 nt
	s_add_u32 s18, s14, 0x6000
	s_addc_u32 s19, s15, 0
	global_load_dwordx4 v[12:15], v208, s[18:19] sc1 nt
	s_add_u32 s18, s14, 0x8000
	s_addc_u32 s19, s15, 0
	global_load_dwordx4 v[16:19], v208, s[18:19] sc1 nt
	s_add_u32 s18, s14, 0xa000
	s_addc_u32 s19, s15, 0
	global_load_dwordx4 v[20:23], v208, s[18:19] sc1 nt
	s_add_u32 s18, s14, 0xc000
	s_addc_u32 s19, s15, 0
	global_load_dwordx4 v[24:27], v208, s[18:19] sc1 nt
	s_add_u32 s18, s14, 0xe000
	s_addc_u32 s19, s15, 0
	global_load_dwordx4 v[28:31], v208, s[18:19] sc1 nt
	s_add_u32 s18, s14, 0x10000
	s_addc_u32 s19, s15, 0
	global_load_dwordx4 v[32:35], v208, s[18:19] sc1 nt
	s_add_u32 s18, s14, 0x12000
	s_addc_u32 s19, s15, 0
	global_load_dwordx4 v[36:39], v208, s[18:19] sc1 nt
	s_add_u32 s18, s14, 0x14000
	s_addc_u32 s19, s15, 0
	global_load_dwordx4 v[40:43], v208, s[18:19] sc1 nt
	s_add_u32 s18, s14, 0x16000
	s_addc_u32 s19, s15, 0
	global_load_dwordx4 v[44:47], v208, s[18:19] sc1 nt
	s_add_u32 s18, s14, 0x18000
	s_addc_u32 s19, s15, 0
	global_load_dwordx4 v[48:51], v208, s[18:19] sc1 nt
	s_add_u32 s18, s14, 0x1a000
	s_addc_u32 s19, s15, 0
	global_load_dwordx4 v[52:55], v208, s[18:19] sc1 nt
	s_add_u32 s18, s14, 0x1c000
	s_addc_u32 s19, s15, 0
	global_load_dwordx4 v[56:59], v208, s[18:19] sc1 nt
	s_add_u32 s18, s14, 0x1e000
	s_addc_u32 s19, s15, 0
	global_load_dwordx4 v[60:63], v208, s[18:19] sc1 nt
	s_add_i32 s1, s20, 4
	s_lshr_b32 s2, s1, 10
	s_and_b32 s4, s1, 0x3ff
	s_lshr_b32 s5, s4, 6
	s_and_b32 s4, s4, 63
	s_lshl_b32 s12, s2, 24
	s_lshl_b32 s13, s5, 20
	s_add_i32 s12, s12, s13
	s_lshl_b32 s13, s4, 7
	s_add_i32 s12, s12, s13
	s_add_u32 s14, s70, s12
	s_addc_u32 s15, s71, 0
	global_load_dwordx4 v[64:67], v208, s[14:15] sc1 nt
	s_add_u32 s18, s14, 0x2000
	s_addc_u32 s19, s15, 0
	global_load_dwordx4 v[68:71], v208, s[18:19] sc1 nt
	s_add_u32 s18, s14, 0x4000
	s_addc_u32 s19, s15, 0
	global_load_dwordx4 v[72:75], v208, s[18:19] sc1 nt
	s_add_u32 s18, s14, 0x6000
	s_addc_u32 s19, s15, 0
	global_load_dwordx4 v[76:79], v208, s[18:19] sc1 nt
	s_add_u32 s18, s14, 0x8000
	s_addc_u32 s19, s15, 0
	global_load_dwordx4 v[80:83], v208, s[18:19] sc1 nt
	s_add_u32 s18, s14, 0xa000
	s_addc_u32 s19, s15, 0
	global_load_dwordx4 v[84:87], v208, s[18:19] sc1 nt
	s_add_u32 s18, s14, 0xc000
	s_addc_u32 s19, s15, 0
	global_load_dwordx4 v[88:91], v208, s[18:19] sc1 nt
	s_add_u32 s18, s14, 0xe000
	s_addc_u32 s19, s15, 0
	global_load_dwordx4 v[92:95], v208, s[18:19] sc1 nt
	s_add_u32 s18, s14, 0x10000
	s_addc_u32 s19, s15, 0
	global_load_dwordx4 v[96:99], v208, s[18:19] sc1 nt
	s_add_u32 s18, s14, 0x12000
	s_addc_u32 s19, s15, 0
	global_load_dwordx4 v[100:103], v208, s[18:19] sc1 nt
	s_add_u32 s18, s14, 0x14000
	s_addc_u32 s19, s15, 0
	global_load_dwordx4 v[104:107], v208, s[18:19] sc1 nt
	s_add_u32 s18, s14, 0x16000
	s_addc_u32 s19, s15, 0
	global_load_dwordx4 v[108:111], v208, s[18:19] sc1 nt
	s_add_u32 s18, s14, 0x18000
	s_addc_u32 s19, s15, 0
	global_load_dwordx4 v[112:115], v208, s[18:19] sc1 nt
	s_add_u32 s18, s14, 0x1a000
	s_addc_u32 s19, s15, 0
	global_load_dwordx4 v[116:119], v208, s[18:19] sc1 nt
	s_add_u32 s18, s14, 0x1c000
	s_addc_u32 s19, s15, 0
	global_load_dwordx4 v[120:123], v208, s[18:19] sc1 nt
	s_add_u32 s18, s14, 0x1e000
	s_addc_u32 s19, s15, 0
	global_load_dwordx4 v[124:127], v208, s[18:19] sc1 nt
	s_add_i32 s1, s20, 8
	s_lshr_b32 s2, s1, 10
	s_and_b32 s4, s1, 0x3ff
	s_lshr_b32 s5, s4, 6
	s_and_b32 s4, s4, 63
	s_lshl_b32 s12, s2, 24
	s_lshl_b32 s13, s5, 20
	s_add_i32 s12, s12, s13
	s_lshl_b32 s13, s4, 7
	s_add_i32 s12, s12, s13
	s_add_u32 s14, s70, s12
	s_addc_u32 s15, s71, 0
	global_load_dwordx4 v[128:131], v208, s[14:15] sc1 nt
	s_add_u32 s18, s14, 0x2000
	s_addc_u32 s19, s15, 0
	global_load_dwordx4 v[132:135], v208, s[18:19] sc1 nt
	s_add_u32 s18, s14, 0x4000
	s_addc_u32 s19, s15, 0
	global_load_dwordx4 v[136:139], v208, s[18:19] sc1 nt
	s_add_u32 s18, s14, 0x6000
	s_addc_u32 s19, s15, 0
	global_load_dwordx4 v[140:143], v208, s[18:19] sc1 nt
	s_add_u32 s18, s14, 0x8000
	s_addc_u32 s19, s15, 0
	global_load_dwordx4 v[144:147], v208, s[18:19] sc1 nt
	s_add_u32 s18, s14, 0xa000
	s_addc_u32 s19, s15, 0
	global_load_dwordx4 v[148:151], v208, s[18:19] sc1 nt
	s_add_u32 s18, s14, 0xc000
	s_addc_u32 s19, s15, 0
	global_load_dwordx4 v[152:155], v208, s[18:19] sc1 nt
	s_add_u32 s18, s14, 0xe000
	s_addc_u32 s19, s15, 0
	global_load_dwordx4 v[156:159], v208, s[18:19] sc1 nt
	s_add_u32 s18, s14, 0x10000
	s_addc_u32 s19, s15, 0
	global_load_dwordx4 v[160:163], v208, s[18:19] sc1 nt
	s_add_u32 s18, s14, 0x12000
	s_addc_u32 s19, s15, 0
	global_load_dwordx4 v[164:167], v208, s[18:19] sc1 nt
	s_add_u32 s18, s14, 0x14000
	s_addc_u32 s19, s15, 0
	global_load_dwordx4 v[168:171], v208, s[18:19] sc1 nt
	s_add_u32 s18, s14, 0x16000
	s_addc_u32 s19, s15, 0
	global_load_dwordx4 v[172:175], v208, s[18:19] sc1 nt
	s_add_u32 s18, s14, 0x18000
	s_addc_u32 s19, s15, 0
	global_load_dwordx4 v[176:179], v208, s[18:19] sc1 nt
	s_add_u32 s18, s14, 0x1a000
	s_addc_u32 s19, s15, 0
	global_load_dwordx4 v[180:183], v208, s[18:19] sc1 nt
	s_add_u32 s18, s14, 0x1c000
	s_addc_u32 s19, s15, 0
	global_load_dwordx4 v[184:187], v208, s[18:19] sc1 nt
	s_add_u32 s18, s14, 0x1e000
	s_addc_u32 s19, s15, 0
	global_load_dwordx4 v[188:191], v208, s[18:19] sc1 nt
	s_waitcnt vmcnt(32)
	s_add_i32 s1, s20, 0
	s_lshr_b32 s2, s1, 10
	s_and_b32 s4, s1, 0x3ff
	s_lshr_b32 s5, s4, 6
	s_and_b32 s4, s4, 63
	s_lshl_b32 s12, s2, 22
	s_lshl_b32 s13, s4, 16
	s_add_i32 s12, s12, s13
	s_lshl_b32 s13, s5, 7
	s_add_i32 s12, s12, s13
	s_add_u32 s24, s90, s12
	s_addc_u32 s25, s91, 0
	s_add_u32 s24, s24, 0x3b100000
	s_addc_u32 s25, s25, 0
	s_add_u32 s26, s24, 0x1000
	s_addc_u32 s27, s25, 0
	v_pk_mul_f32 v[0:1], v[0:1], s[16:17] op_sel_hi:[1,0]
	v_pk_mul_f32 v[2:3], v[2:3], s[16:17] op_sel_hi:[1,0]
	v_pk_mul_f32 v[4:5], v[4:5], s[16:17] op_sel_hi:[1,0]
	v_pk_mul_f32 v[6:7], v[6:7], s[16:17] op_sel_hi:[1,0]
	v_pk_mul_f32 v[8:9], v[8:9], s[16:17] op_sel_hi:[1,0]
	v_pk_mul_f32 v[10:11], v[10:11], s[16:17] op_sel_hi:[1,0]
	v_pk_mul_f32 v[12:13], v[12:13], s[16:17] op_sel_hi:[1,0]
	v_pk_mul_f32 v[14:15], v[14:15], s[16:17] op_sel_hi:[1,0]
	v_pk_mul_f32 v[16:17], v[16:17], s[16:17] op_sel_hi:[1,0]
	v_pk_mul_f32 v[18:19], v[18:19], s[16:17] op_sel_hi:[1,0]
	v_pk_mul_f32 v[20:21], v[20:21], s[16:17] op_sel_hi:[1,0]
	v_pk_mul_f32 v[22:23], v[22:23], s[16:17] op_sel_hi:[1,0]
	v_pk_mul_f32 v[24:25], v[24:25], s[16:17] op_sel_hi:[1,0]
	v_pk_mul_f32 v[26:27], v[26:27], s[16:17] op_sel_hi:[1,0]
	v_pk_mul_f32 v[28:29], v[28:29], s[16:17] op_sel_hi:[1,0]
	v_pk_mul_f32 v[30:31], v[30:31], s[16:17] op_sel_hi:[1,0]
	v_pk_mul_f32 v[32:33], v[32:33], s[16:17] op_sel_hi:[1,0]
	v_pk_mul_f32 v[34:35], v[34:35], s[16:17] op_sel_hi:[1,0]
	v_pk_mul_f32 v[36:37], v[36:37], s[16:17] op_sel_hi:[1,0]
	v_pk_mul_f32 v[38:39], v[38:39], s[16:17] op_sel_hi:[1,0]
	v_pk_mul_f32 v[40:41], v[40:41], s[16:17] op_sel_hi:[1,0]
	v_pk_mul_f32 v[42:43], v[42:43], s[16:17] op_sel_hi:[1,0]
	v_pk_mul_f32 v[44:45], v[44:45], s[16:17] op_sel_hi:[1,0]
	v_pk_mul_f32 v[46:47], v[46:47], s[16:17] op_sel_hi:[1,0]
	v_pk_mul_f32 v[48:49], v[48:49], s[16:17] op_sel_hi:[1,0]
	v_pk_mul_f32 v[50:51], v[50:51], s[16:17] op_sel_hi:[1,0]
	v_pk_mul_f32 v[52:53], v[52:53], s[16:17] op_sel_hi:[1,0]
	v_pk_mul_f32 v[54:55], v[54:55], s[16:17] op_sel_hi:[1,0]
	v_pk_mul_f32 v[56:57], v[56:57], s[16:17] op_sel_hi:[1,0]
	v_pk_mul_f32 v[58:59], v[58:59], s[16:17] op_sel_hi:[1,0]
	v_pk_mul_f32 v[60:61], v[60:61], s[16:17] op_sel_hi:[1,0]
	v_pk_mul_f32 v[62:63], v[62:63], s[16:17] op_sel_hi:[1,0]
	v_cvt_pk_fp8_f32 v192, v0, v4
	v_cvt_pk_fp8_f32 v192, v8, v12 op_sel:[0,0,1]
	v_cvt_pk_fp8_f32 v193, v16, v20
	v_cvt_pk_fp8_f32 v193, v24, v28 op_sel:[0,0,1]
	v_cvt_pk_fp8_f32 v194, v32, v36
	v_cvt_pk_fp8_f32 v194, v40, v44 op_sel:[0,0,1]
	v_cvt_pk_fp8_f32 v195, v48, v52
	v_cvt_pk_fp8_f32 v195, v56, v60 op_sel:[0,0,1]
	global_store_dwordx4 v209, v[192:195], s[24:25] sc1
	v_cvt_pk_fp8_f32 v196, v1, v5
	v_cvt_pk_fp8_f32 v196, v9, v13 op_sel:[0,0,1]
	v_cvt_pk_fp8_f32 v197, v17, v21
	v_cvt_pk_fp8_f32 v197, v25, v29 op_sel:[0,0,1]
	v_cvt_pk_fp8_f32 v198, v33, v37
	v_cvt_pk_fp8_f32 v198, v41, v45 op_sel:[0,0,1]
	v_cvt_pk_fp8_f32 v199, v49, v53
	v_cvt_pk_fp8_f32 v199, v57, v61 op_sel:[0,0,1]
	global_store_dwordx4 v209, v[196:199], s[24:25] offset:2048 sc1
	v_cvt_pk_fp8_f32 v200, v2, v6
	v_cvt_pk_fp8_f32 v200, v10, v14 op_sel:[0,0,1]
	v_cvt_pk_fp8_f32 v201, v18, v22
	v_cvt_pk_fp8_f32 v201, v26, v30 op_sel:[0,0,1]
	v_cvt_pk_fp8_f32 v202, v34, v38
	v_cvt_pk_fp8_f32 v202, v42, v46 op_sel:[0,0,1]
	v_cvt_pk_fp8_f32 v203, v50, v54
	v_cvt_pk_fp8_f32 v203, v58, v62 op_sel:[0,0,1]
	global_store_dwordx4 v209, v[200:203], s[26:27] sc1
	v_cvt_pk_fp8_f32 v204, v3, v7
	v_cvt_pk_fp8_f32 v204, v11, v15 op_sel:[0,0,1]
	v_cvt_pk_fp8_f32 v205, v19, v23
	v_cvt_pk_fp8_f32 v205, v27, v31 op_sel:[0,0,1]
	v_cvt_pk_fp8_f32 v206, v35, v39
	v_cvt_pk_fp8_f32 v206, v43, v47 op_sel:[0,0,1]
	v_cvt_pk_fp8_f32 v207, v51, v55
	v_cvt_pk_fp8_f32 v207, v59, v63 op_sel:[0,0,1]
	global_store_dwordx4 v209, v[204:207], s[26:27] offset:2048 sc1
	s_add_i32 s1, s20, 12
	s_lshr_b32 s2, s1, 10
	s_and_b32 s4, s1, 0x3ff
	s_lshr_b32 s5, s4, 6
	s_and_b32 s4, s4, 63
	s_lshl_b32 s12, s2, 24
	s_lshl_b32 s13, s5, 20
	s_add_i32 s12, s12, s13
	s_lshl_b32 s13, s4, 7
	s_add_i32 s12, s12, s13
	s_add_u32 s14, s70, s12
	s_addc_u32 s15, s71, 0
	global_load_dwordx4 v[0:3], v208, s[14:15] sc1 nt
	s_add_u32 s18, s14, 0x2000
	s_addc_u32 s19, s15, 0
	global_load_dwordx4 v[4:7], v208, s[18:19] sc1 nt
	s_add_u32 s18, s14, 0x4000
	s_addc_u32 s19, s15, 0
	global_load_dwordx4 v[8:11], v208, s[18:19] sc1 nt
	s_add_u32 s18, s14, 0x6000
	s_addc_u32 s19, s15, 0
	global_load_dwordx4 v[12:15], v208, s[18:19] sc1 nt
	s_add_u32 s18, s14, 0x8000
	s_addc_u32 s19, s15, 0
	global_load_dwordx4 v[16:19], v208, s[18:19] sc1 nt
	s_add_u32 s18, s14, 0xa000
	s_addc_u32 s19, s15, 0
	global_load_dwordx4 v[20:23], v208, s[18:19] sc1 nt
	s_add_u32 s18, s14, 0xc000
	s_addc_u32 s19, s15, 0
	global_load_dwordx4 v[24:27], v208, s[18:19] sc1 nt
	s_add_u32 s18, s14, 0xe000
	s_addc_u32 s19, s15, 0
	global_load_dwordx4 v[28:31], v208, s[18:19] sc1 nt
	s_add_u32 s18, s14, 0x10000
	s_addc_u32 s19, s15, 0
	global_load_dwordx4 v[32:35], v208, s[18:19] sc1 nt
	s_add_u32 s18, s14, 0x12000
	s_addc_u32 s19, s15, 0
	global_load_dwordx4 v[36:39], v208, s[18:19] sc1 nt
	s_add_u32 s18, s14, 0x14000
	s_addc_u32 s19, s15, 0
	global_load_dwordx4 v[40:43], v208, s[18:19] sc1 nt
	s_add_u32 s18, s14, 0x16000
	s_addc_u32 s19, s15, 0
	global_load_dwordx4 v[44:47], v208, s[18:19] sc1 nt
	s_add_u32 s18, s14, 0x18000
	s_addc_u32 s19, s15, 0
	global_load_dwordx4 v[48:51], v208, s[18:19] sc1 nt
	s_add_u32 s18, s14, 0x1a000
	s_addc_u32 s19, s15, 0
	global_load_dwordx4 v[52:55], v208, s[18:19] sc1 nt
	s_add_u32 s18, s14, 0x1c000
	s_addc_u32 s19, s15, 0
	global_load_dwordx4 v[56:59], v208, s[18:19] sc1 nt
	s_add_u32 s18, s14, 0x1e000
	s_addc_u32 s19, s15, 0
	global_load_dwordx4 v[60:63], v208, s[18:19] sc1 nt
	s_waitcnt vmcnt(36)
	s_add_i32 s1, s20, 4
	s_lshr_b32 s2, s1, 10
	s_and_b32 s4, s1, 0x3ff
	s_lshr_b32 s5, s4, 6
	s_and_b32 s4, s4, 63
	s_lshl_b32 s12, s2, 22
	s_lshl_b32 s13, s4, 16
	s_add_i32 s12, s12, s13
	s_lshl_b32 s13, s5, 7
	s_add_i32 s12, s12, s13
	s_add_u32 s24, s90, s12
	s_addc_u32 s25, s91, 0
	s_add_u32 s24, s24, 0x3b100000
	s_addc_u32 s25, s25, 0
	s_add_u32 s26, s24, 0x1000
	s_addc_u32 s27, s25, 0
	v_pk_mul_f32 v[64:65], v[64:65], s[16:17] op_sel_hi:[1,0]
	v_pk_mul_f32 v[66:67], v[66:67], s[16:17] op_sel_hi:[1,0]
	v_pk_mul_f32 v[68:69], v[68:69], s[16:17] op_sel_hi:[1,0]
	v_pk_mul_f32 v[70:71], v[70:71], s[16:17] op_sel_hi:[1,0]
	v_pk_mul_f32 v[72:73], v[72:73], s[16:17] op_sel_hi:[1,0]
	v_pk_mul_f32 v[74:75], v[74:75], s[16:17] op_sel_hi:[1,0]
	v_pk_mul_f32 v[76:77], v[76:77], s[16:17] op_sel_hi:[1,0]
	v_pk_mul_f32 v[78:79], v[78:79], s[16:17] op_sel_hi:[1,0]
	v_pk_mul_f32 v[80:81], v[80:81], s[16:17] op_sel_hi:[1,0]
	v_pk_mul_f32 v[82:83], v[82:83], s[16:17] op_sel_hi:[1,0]
	v_pk_mul_f32 v[84:85], v[84:85], s[16:17] op_sel_hi:[1,0]
	v_pk_mul_f32 v[86:87], v[86:87], s[16:17] op_sel_hi:[1,0]
	v_pk_mul_f32 v[88:89], v[88:89], s[16:17] op_sel_hi:[1,0]
	v_pk_mul_f32 v[90:91], v[90:91], s[16:17] op_sel_hi:[1,0]
	v_pk_mul_f32 v[92:93], v[92:93], s[16:17] op_sel_hi:[1,0]
	v_pk_mul_f32 v[94:95], v[94:95], s[16:17] op_sel_hi:[1,0]
	v_pk_mul_f32 v[96:97], v[96:97], s[16:17] op_sel_hi:[1,0]
	v_pk_mul_f32 v[98:99], v[98:99], s[16:17] op_sel_hi:[1,0]
	v_pk_mul_f32 v[100:101], v[100:101], s[16:17] op_sel_hi:[1,0]
	v_pk_mul_f32 v[102:103], v[102:103], s[16:17] op_sel_hi:[1,0]
	v_pk_mul_f32 v[104:105], v[104:105], s[16:17] op_sel_hi:[1,0]
	v_pk_mul_f32 v[106:107], v[106:107], s[16:17] op_sel_hi:[1,0]
	v_pk_mul_f32 v[108:109], v[108:109], s[16:17] op_sel_hi:[1,0]
	v_pk_mul_f32 v[110:111], v[110:111], s[16:17] op_sel_hi:[1,0]
	v_pk_mul_f32 v[112:113], v[112:113], s[16:17] op_sel_hi:[1,0]
	v_pk_mul_f32 v[114:115], v[114:115], s[16:17] op_sel_hi:[1,0]
	v_pk_mul_f32 v[116:117], v[116:117], s[16:17] op_sel_hi:[1,0]
	v_pk_mul_f32 v[118:119], v[118:119], s[16:17] op_sel_hi:[1,0]
	v_pk_mul_f32 v[120:121], v[120:121], s[16:17] op_sel_hi:[1,0]
	v_pk_mul_f32 v[122:123], v[122:123], s[16:17] op_sel_hi:[1,0]
	v_pk_mul_f32 v[124:125], v[124:125], s[16:17] op_sel_hi:[1,0]
	v_pk_mul_f32 v[126:127], v[126:127], s[16:17] op_sel_hi:[1,0]
	v_cvt_pk_fp8_f32 v192, v64, v68
	v_cvt_pk_fp8_f32 v192, v72, v76 op_sel:[0,0,1]
	v_cvt_pk_fp8_f32 v193, v80, v84
	v_cvt_pk_fp8_f32 v193, v88, v92 op_sel:[0,0,1]
	v_cvt_pk_fp8_f32 v194, v96, v100
	v_cvt_pk_fp8_f32 v194, v104, v108 op_sel:[0,0,1]
	v_cvt_pk_fp8_f32 v195, v112, v116
	v_cvt_pk_fp8_f32 v195, v120, v124 op_sel:[0,0,1]
	global_store_dwordx4 v209, v[192:195], s[24:25] sc1
	v_cvt_pk_fp8_f32 v196, v65, v69
	v_cvt_pk_fp8_f32 v196, v73, v77 op_sel:[0,0,1]
	v_cvt_pk_fp8_f32 v197, v81, v85
	v_cvt_pk_fp8_f32 v197, v89, v93 op_sel:[0,0,1]
	v_cvt_pk_fp8_f32 v198, v97, v101
	v_cvt_pk_fp8_f32 v198, v105, v109 op_sel:[0,0,1]
	v_cvt_pk_fp8_f32 v199, v113, v117
	v_cvt_pk_fp8_f32 v199, v121, v125 op_sel:[0,0,1]
	global_store_dwordx4 v209, v[196:199], s[24:25] offset:2048 sc1
	v_cvt_pk_fp8_f32 v200, v66, v70
	v_cvt_pk_fp8_f32 v200, v74, v78 op_sel:[0,0,1]
	v_cvt_pk_fp8_f32 v201, v82, v86
	v_cvt_pk_fp8_f32 v201, v90, v94 op_sel:[0,0,1]
	v_cvt_pk_fp8_f32 v202, v98, v102
	v_cvt_pk_fp8_f32 v202, v106, v110 op_sel:[0,0,1]
	v_cvt_pk_fp8_f32 v203, v114, v118
	v_cvt_pk_fp8_f32 v203, v122, v126 op_sel:[0,0,1]
	global_store_dwordx4 v209, v[200:203], s[26:27] sc1
	v_cvt_pk_fp8_f32 v204, v67, v71
	v_cvt_pk_fp8_f32 v204, v75, v79 op_sel:[0,0,1]
	v_cvt_pk_fp8_f32 v205, v83, v87
	v_cvt_pk_fp8_f32 v205, v91, v95 op_sel:[0,0,1]
	v_cvt_pk_fp8_f32 v206, v99, v103
	v_cvt_pk_fp8_f32 v206, v107, v111 op_sel:[0,0,1]
	v_cvt_pk_fp8_f32 v207, v115, v119
	v_cvt_pk_fp8_f32 v207, v123, v127 op_sel:[0,0,1]
	global_store_dwordx4 v209, v[204:207], s[26:27] offset:2048 sc1
	s_add_i32 s1, s20, 16
	s_lshr_b32 s2, s1, 10
	s_and_b32 s4, s1, 0x3ff
	s_lshr_b32 s5, s4, 6
	s_and_b32 s4, s4, 63
	s_lshl_b32 s12, s2, 24
	s_lshl_b32 s13, s5, 20
	s_add_i32 s12, s12, s13
	s_lshl_b32 s13, s4, 7
	s_add_i32 s12, s12, s13
	s_add_u32 s14, s70, s12
	s_addc_u32 s15, s71, 0
	global_load_dwordx4 v[64:67], v208, s[14:15] sc1 nt
	s_add_u32 s18, s14, 0x2000
	s_addc_u32 s19, s15, 0
	global_load_dwordx4 v[68:71], v208, s[18:19] sc1 nt
	s_add_u32 s18, s14, 0x4000
	s_addc_u32 s19, s15, 0
	global_load_dwordx4 v[72:75], v208, s[18:19] sc1 nt
	s_add_u32 s18, s14, 0x6000
	s_addc_u32 s19, s15, 0
	global_load_dwordx4 v[76:79], v208, s[18:19] sc1 nt
	s_add_u32 s18, s14, 0x8000
	s_addc_u32 s19, s15, 0
	global_load_dwordx4 v[80:83], v208, s[18:19] sc1 nt
	s_add_u32 s18, s14, 0xa000
	s_addc_u32 s19, s15, 0
	global_load_dwordx4 v[84:87], v208, s[18:19] sc1 nt
	s_add_u32 s18, s14, 0xc000
	s_addc_u32 s19, s15, 0
	global_load_dwordx4 v[88:91], v208, s[18:19] sc1 nt
	s_add_u32 s18, s14, 0xe000
	s_addc_u32 s19, s15, 0
	global_load_dwordx4 v[92:95], v208, s[18:19] sc1 nt
	s_add_u32 s18, s14, 0x10000
	s_addc_u32 s19, s15, 0
	global_load_dwordx4 v[96:99], v208, s[18:19] sc1 nt
	s_add_u32 s18, s14, 0x12000
	s_addc_u32 s19, s15, 0
	global_load_dwordx4 v[100:103], v208, s[18:19] sc1 nt
	s_add_u32 s18, s14, 0x14000
	s_addc_u32 s19, s15, 0
	global_load_dwordx4 v[104:107], v208, s[18:19] sc1 nt
	s_add_u32 s18, s14, 0x16000
	s_addc_u32 s19, s15, 0
	global_load_dwordx4 v[108:111], v208, s[18:19] sc1 nt
	s_add_u32 s18, s14, 0x18000
	s_addc_u32 s19, s15, 0
	global_load_dwordx4 v[112:115], v208, s[18:19] sc1 nt
	s_add_u32 s18, s14, 0x1a000
	s_addc_u32 s19, s15, 0
	global_load_dwordx4 v[116:119], v208, s[18:19] sc1 nt
	s_add_u32 s18, s14, 0x1c000
	s_addc_u32 s19, s15, 0
	global_load_dwordx4 v[120:123], v208, s[18:19] sc1 nt
	s_add_u32 s18, s14, 0x1e000
	s_addc_u32 s19, s15, 0
	global_load_dwordx4 v[124:127], v208, s[18:19] sc1 nt
	s_waitcnt vmcnt(40)
	s_add_i32 s1, s20, 8
	s_lshr_b32 s2, s1, 10
	s_and_b32 s4, s1, 0x3ff
	s_lshr_b32 s5, s4, 6
	s_and_b32 s4, s4, 63
	s_lshl_b32 s12, s2, 22
	s_lshl_b32 s13, s4, 16
	s_add_i32 s12, s12, s13
	s_lshl_b32 s13, s5, 7
	s_add_i32 s12, s12, s13
	s_add_u32 s24, s90, s12
	s_addc_u32 s25, s91, 0
	s_add_u32 s24, s24, 0x3b100000
	s_addc_u32 s25, s25, 0
	s_add_u32 s26, s24, 0x1000
	s_addc_u32 s27, s25, 0
	v_pk_mul_f32 v[128:129], v[128:129], s[16:17] op_sel_hi:[1,0]
	v_pk_mul_f32 v[130:131], v[130:131], s[16:17] op_sel_hi:[1,0]
	v_pk_mul_f32 v[132:133], v[132:133], s[16:17] op_sel_hi:[1,0]
	v_pk_mul_f32 v[134:135], v[134:135], s[16:17] op_sel_hi:[1,0]
	v_pk_mul_f32 v[136:137], v[136:137], s[16:17] op_sel_hi:[1,0]
	v_pk_mul_f32 v[138:139], v[138:139], s[16:17] op_sel_hi:[1,0]
	v_pk_mul_f32 v[140:141], v[140:141], s[16:17] op_sel_hi:[1,0]
	v_pk_mul_f32 v[142:143], v[142:143], s[16:17] op_sel_hi:[1,0]
	v_pk_mul_f32 v[144:145], v[144:145], s[16:17] op_sel_hi:[1,0]
	v_pk_mul_f32 v[146:147], v[146:147], s[16:17] op_sel_hi:[1,0]
	v_pk_mul_f32 v[148:149], v[148:149], s[16:17] op_sel_hi:[1,0]
	v_pk_mul_f32 v[150:151], v[150:151], s[16:17] op_sel_hi:[1,0]
	v_pk_mul_f32 v[152:153], v[152:153], s[16:17] op_sel_hi:[1,0]
	v_pk_mul_f32 v[154:155], v[154:155], s[16:17] op_sel_hi:[1,0]
	v_pk_mul_f32 v[156:157], v[156:157], s[16:17] op_sel_hi:[1,0]
	v_pk_mul_f32 v[158:159], v[158:159], s[16:17] op_sel_hi:[1,0]
	v_pk_mul_f32 v[160:161], v[160:161], s[16:17] op_sel_hi:[1,0]
	v_pk_mul_f32 v[162:163], v[162:163], s[16:17] op_sel_hi:[1,0]
	v_pk_mul_f32 v[164:165], v[164:165], s[16:17] op_sel_hi:[1,0]
	v_pk_mul_f32 v[166:167], v[166:167], s[16:17] op_sel_hi:[1,0]
	v_pk_mul_f32 v[168:169], v[168:169], s[16:17] op_sel_hi:[1,0]
	v_pk_mul_f32 v[170:171], v[170:171], s[16:17] op_sel_hi:[1,0]
	v_pk_mul_f32 v[172:173], v[172:173], s[16:17] op_sel_hi:[1,0]
	v_pk_mul_f32 v[174:175], v[174:175], s[16:17] op_sel_hi:[1,0]
	v_pk_mul_f32 v[176:177], v[176:177], s[16:17] op_sel_hi:[1,0]
	v_pk_mul_f32 v[178:179], v[178:179], s[16:17] op_sel_hi:[1,0]
	v_pk_mul_f32 v[180:181], v[180:181], s[16:17] op_sel_hi:[1,0]
	v_pk_mul_f32 v[182:183], v[182:183], s[16:17] op_sel_hi:[1,0]
	v_pk_mul_f32 v[184:185], v[184:185], s[16:17] op_sel_hi:[1,0]
	v_pk_mul_f32 v[186:187], v[186:187], s[16:17] op_sel_hi:[1,0]
	v_pk_mul_f32 v[188:189], v[188:189], s[16:17] op_sel_hi:[1,0]
	v_pk_mul_f32 v[190:191], v[190:191], s[16:17] op_sel_hi:[1,0]
	v_cvt_pk_fp8_f32 v192, v128, v132
	v_cvt_pk_fp8_f32 v192, v136, v140 op_sel:[0,0,1]
	v_cvt_pk_fp8_f32 v193, v144, v148
	v_cvt_pk_fp8_f32 v193, v152, v156 op_sel:[0,0,1]
	v_cvt_pk_fp8_f32 v194, v160, v164
	v_cvt_pk_fp8_f32 v194, v168, v172 op_sel:[0,0,1]
	v_cvt_pk_fp8_f32 v195, v176, v180
	v_cvt_pk_fp8_f32 v195, v184, v188 op_sel:[0,0,1]
	global_store_dwordx4 v209, v[192:195], s[24:25] sc1
	v_cvt_pk_fp8_f32 v196, v129, v133
	v_cvt_pk_fp8_f32 v196, v137, v141 op_sel:[0,0,1]
	v_cvt_pk_fp8_f32 v197, v145, v149
	v_cvt_pk_fp8_f32 v197, v153, v157 op_sel:[0,0,1]
	v_cvt_pk_fp8_f32 v198, v161, v165
	v_cvt_pk_fp8_f32 v198, v169, v173 op_sel:[0,0,1]
	v_cvt_pk_fp8_f32 v199, v177, v181
	v_cvt_pk_fp8_f32 v199, v185, v189 op_sel:[0,0,1]
	global_store_dwordx4 v209, v[196:199], s[24:25] offset:2048 sc1
	v_cvt_pk_fp8_f32 v200, v130, v134
	v_cvt_pk_fp8_f32 v200, v138, v142 op_sel:[0,0,1]
	v_cvt_pk_fp8_f32 v201, v146, v150
	v_cvt_pk_fp8_f32 v201, v154, v158 op_sel:[0,0,1]
	v_cvt_pk_fp8_f32 v202, v162, v166
	v_cvt_pk_fp8_f32 v202, v170, v174 op_sel:[0,0,1]
	v_cvt_pk_fp8_f32 v203, v178, v182
	v_cvt_pk_fp8_f32 v203, v186, v190 op_sel:[0,0,1]
	global_store_dwordx4 v209, v[200:203], s[26:27] sc1
	v_cvt_pk_fp8_f32 v204, v131, v135
	v_cvt_pk_fp8_f32 v204, v139, v143 op_sel:[0,0,1]
	v_cvt_pk_fp8_f32 v205, v147, v151
	v_cvt_pk_fp8_f32 v205, v155, v159 op_sel:[0,0,1]
	v_cvt_pk_fp8_f32 v206, v163, v167
	v_cvt_pk_fp8_f32 v206, v171, v175 op_sel:[0,0,1]
	v_cvt_pk_fp8_f32 v207, v179, v183
	v_cvt_pk_fp8_f32 v207, v187, v191 op_sel:[0,0,1]
	global_store_dwordx4 v209, v[204:207], s[26:27] offset:2048 sc1
	s_add_i32 s1, s20, 20
	s_lshr_b32 s2, s1, 10
	s_and_b32 s4, s1, 0x3ff
	s_lshr_b32 s5, s4, 6
	s_and_b32 s4, s4, 63
	s_lshl_b32 s12, s2, 24
	s_lshl_b32 s13, s5, 20
	s_add_i32 s12, s12, s13
	s_lshl_b32 s13, s4, 7
	s_add_i32 s12, s12, s13
	s_add_u32 s14, s70, s12
	s_addc_u32 s15, s71, 0
	global_load_dwordx4 v[128:131], v208, s[14:15] sc1 nt
	s_add_u32 s18, s14, 0x2000
	s_addc_u32 s19, s15, 0
	global_load_dwordx4 v[132:135], v208, s[18:19] sc1 nt
	s_add_u32 s18, s14, 0x4000
	s_addc_u32 s19, s15, 0
	global_load_dwordx4 v[136:139], v208, s[18:19] sc1 nt
	s_add_u32 s18, s14, 0x6000
	s_addc_u32 s19, s15, 0
	global_load_dwordx4 v[140:143], v208, s[18:19] sc1 nt
	s_add_u32 s18, s14, 0x8000
	s_addc_u32 s19, s15, 0
	global_load_dwordx4 v[144:147], v208, s[18:19] sc1 nt
	s_add_u32 s18, s14, 0xa000
	s_addc_u32 s19, s15, 0
	global_load_dwordx4 v[148:151], v208, s[18:19] sc1 nt
	s_add_u32 s18, s14, 0xc000
	s_addc_u32 s19, s15, 0
	global_load_dwordx4 v[152:155], v208, s[18:19] sc1 nt
	s_add_u32 s18, s14, 0xe000
	s_addc_u32 s19, s15, 0
	global_load_dwordx4 v[156:159], v208, s[18:19] sc1 nt
	s_add_u32 s18, s14, 0x10000
	s_addc_u32 s19, s15, 0
	global_load_dwordx4 v[160:163], v208, s[18:19] sc1 nt
	s_add_u32 s18, s14, 0x12000
	s_addc_u32 s19, s15, 0
	global_load_dwordx4 v[164:167], v208, s[18:19] sc1 nt
	s_add_u32 s18, s14, 0x14000
	s_addc_u32 s19, s15, 0
	global_load_dwordx4 v[168:171], v208, s[18:19] sc1 nt
	s_add_u32 s18, s14, 0x16000
	s_addc_u32 s19, s15, 0
	global_load_dwordx4 v[172:175], v208, s[18:19] sc1 nt
	s_add_u32 s18, s14, 0x18000
	s_addc_u32 s19, s15, 0
	global_load_dwordx4 v[176:179], v208, s[18:19] sc1 nt
	s_add_u32 s18, s14, 0x1a000
	s_addc_u32 s19, s15, 0
	global_load_dwordx4 v[180:183], v208, s[18:19] sc1 nt
	s_add_u32 s18, s14, 0x1c000
	s_addc_u32 s19, s15, 0
	global_load_dwordx4 v[184:187], v208, s[18:19] sc1 nt
	s_add_u32 s18, s14, 0x1e000
	s_addc_u32 s19, s15, 0
	global_load_dwordx4 v[188:191], v208, s[18:19] sc1 nt
	s_waitcnt vmcnt(40)
	s_add_i32 s1, s20, 12
	s_lshr_b32 s2, s1, 10
	s_and_b32 s4, s1, 0x3ff
	s_lshr_b32 s5, s4, 6
	s_and_b32 s4, s4, 63
	s_lshl_b32 s12, s2, 22
	s_lshl_b32 s13, s4, 16
	s_add_i32 s12, s12, s13
	s_lshl_b32 s13, s5, 7
	s_add_i32 s12, s12, s13
	s_add_u32 s24, s90, s12
	s_addc_u32 s25, s91, 0
	s_add_u32 s24, s24, 0x3b100000
	s_addc_u32 s25, s25, 0
	s_add_u32 s26, s24, 0x1000
	s_addc_u32 s27, s25, 0
	v_pk_mul_f32 v[0:1], v[0:1], s[16:17] op_sel_hi:[1,0]
	v_pk_mul_f32 v[2:3], v[2:3], s[16:17] op_sel_hi:[1,0]
	v_pk_mul_f32 v[4:5], v[4:5], s[16:17] op_sel_hi:[1,0]
	v_pk_mul_f32 v[6:7], v[6:7], s[16:17] op_sel_hi:[1,0]
	v_pk_mul_f32 v[8:9], v[8:9], s[16:17] op_sel_hi:[1,0]
	v_pk_mul_f32 v[10:11], v[10:11], s[16:17] op_sel_hi:[1,0]
	v_pk_mul_f32 v[12:13], v[12:13], s[16:17] op_sel_hi:[1,0]
	v_pk_mul_f32 v[14:15], v[14:15], s[16:17] op_sel_hi:[1,0]
	v_pk_mul_f32 v[16:17], v[16:17], s[16:17] op_sel_hi:[1,0]
	v_pk_mul_f32 v[18:19], v[18:19], s[16:17] op_sel_hi:[1,0]
	v_pk_mul_f32 v[20:21], v[20:21], s[16:17] op_sel_hi:[1,0]
	v_pk_mul_f32 v[22:23], v[22:23], s[16:17] op_sel_hi:[1,0]
	v_pk_mul_f32 v[24:25], v[24:25], s[16:17] op_sel_hi:[1,0]
	v_pk_mul_f32 v[26:27], v[26:27], s[16:17] op_sel_hi:[1,0]
	v_pk_mul_f32 v[28:29], v[28:29], s[16:17] op_sel_hi:[1,0]
	v_pk_mul_f32 v[30:31], v[30:31], s[16:17] op_sel_hi:[1,0]
	v_pk_mul_f32 v[32:33], v[32:33], s[16:17] op_sel_hi:[1,0]
	v_pk_mul_f32 v[34:35], v[34:35], s[16:17] op_sel_hi:[1,0]
	v_pk_mul_f32 v[36:37], v[36:37], s[16:17] op_sel_hi:[1,0]
	v_pk_mul_f32 v[38:39], v[38:39], s[16:17] op_sel_hi:[1,0]
	v_pk_mul_f32 v[40:41], v[40:41], s[16:17] op_sel_hi:[1,0]
	v_pk_mul_f32 v[42:43], v[42:43], s[16:17] op_sel_hi:[1,0]
	v_pk_mul_f32 v[44:45], v[44:45], s[16:17] op_sel_hi:[1,0]
	v_pk_mul_f32 v[46:47], v[46:47], s[16:17] op_sel_hi:[1,0]
	v_pk_mul_f32 v[48:49], v[48:49], s[16:17] op_sel_hi:[1,0]
	v_pk_mul_f32 v[50:51], v[50:51], s[16:17] op_sel_hi:[1,0]
	v_pk_mul_f32 v[52:53], v[52:53], s[16:17] op_sel_hi:[1,0]
	v_pk_mul_f32 v[54:55], v[54:55], s[16:17] op_sel_hi:[1,0]
	v_pk_mul_f32 v[56:57], v[56:57], s[16:17] op_sel_hi:[1,0]
	v_pk_mul_f32 v[58:59], v[58:59], s[16:17] op_sel_hi:[1,0]
	v_pk_mul_f32 v[60:61], v[60:61], s[16:17] op_sel_hi:[1,0]
	v_pk_mul_f32 v[62:63], v[62:63], s[16:17] op_sel_hi:[1,0]
	v_cvt_pk_fp8_f32 v192, v0, v4
	v_cvt_pk_fp8_f32 v192, v8, v12 op_sel:[0,0,1]
	v_cvt_pk_fp8_f32 v193, v16, v20
	v_cvt_pk_fp8_f32 v193, v24, v28 op_sel:[0,0,1]
	v_cvt_pk_fp8_f32 v194, v32, v36
	v_cvt_pk_fp8_f32 v194, v40, v44 op_sel:[0,0,1]
	v_cvt_pk_fp8_f32 v195, v48, v52
	v_cvt_pk_fp8_f32 v195, v56, v60 op_sel:[0,0,1]
	global_store_dwordx4 v209, v[192:195], s[24:25] sc1
	v_cvt_pk_fp8_f32 v196, v1, v5
	v_cvt_pk_fp8_f32 v196, v9, v13 op_sel:[0,0,1]
	v_cvt_pk_fp8_f32 v197, v17, v21
	v_cvt_pk_fp8_f32 v197, v25, v29 op_sel:[0,0,1]
	v_cvt_pk_fp8_f32 v198, v33, v37
	v_cvt_pk_fp8_f32 v198, v41, v45 op_sel:[0,0,1]
	v_cvt_pk_fp8_f32 v199, v49, v53
	v_cvt_pk_fp8_f32 v199, v57, v61 op_sel:[0,0,1]
	global_store_dwordx4 v209, v[196:199], s[24:25] offset:2048 sc1
	v_cvt_pk_fp8_f32 v200, v2, v6
	v_cvt_pk_fp8_f32 v200, v10, v14 op_sel:[0,0,1]
	v_cvt_pk_fp8_f32 v201, v18, v22
	v_cvt_pk_fp8_f32 v201, v26, v30 op_sel:[0,0,1]
	v_cvt_pk_fp8_f32 v202, v34, v38
	v_cvt_pk_fp8_f32 v202, v42, v46 op_sel:[0,0,1]
	v_cvt_pk_fp8_f32 v203, v50, v54
	v_cvt_pk_fp8_f32 v203, v58, v62 op_sel:[0,0,1]
	global_store_dwordx4 v209, v[200:203], s[26:27] sc1
	v_cvt_pk_fp8_f32 v204, v3, v7
	v_cvt_pk_fp8_f32 v204, v11, v15 op_sel:[0,0,1]
	v_cvt_pk_fp8_f32 v205, v19, v23
	v_cvt_pk_fp8_f32 v205, v27, v31 op_sel:[0,0,1]
	v_cvt_pk_fp8_f32 v206, v35, v39
	v_cvt_pk_fp8_f32 v206, v43, v47 op_sel:[0,0,1]
	v_cvt_pk_fp8_f32 v207, v51, v55
	v_cvt_pk_fp8_f32 v207, v59, v63 op_sel:[0,0,1]
	global_store_dwordx4 v209, v[204:207], s[26:27] offset:2048 sc1
	s_add_i32 s1, s20, 24
	s_lshr_b32 s2, s1, 10
	s_and_b32 s4, s1, 0x3ff
	s_lshr_b32 s5, s4, 6
	s_and_b32 s4, s4, 63
	s_lshl_b32 s12, s2, 24
	s_lshl_b32 s13, s5, 20
	s_add_i32 s12, s12, s13
	s_lshl_b32 s13, s4, 7
	s_add_i32 s12, s12, s13
	s_add_u32 s14, s70, s12
	s_addc_u32 s15, s71, 0
	global_load_dwordx4 v[0:3], v208, s[14:15] sc1 nt
	s_add_u32 s18, s14, 0x2000
	s_addc_u32 s19, s15, 0
	global_load_dwordx4 v[4:7], v208, s[18:19] sc1 nt
	s_add_u32 s18, s14, 0x4000
	s_addc_u32 s19, s15, 0
	global_load_dwordx4 v[8:11], v208, s[18:19] sc1 nt
	s_add_u32 s18, s14, 0x6000
	s_addc_u32 s19, s15, 0
	global_load_dwordx4 v[12:15], v208, s[18:19] sc1 nt
	s_add_u32 s18, s14, 0x8000
	s_addc_u32 s19, s15, 0
	global_load_dwordx4 v[16:19], v208, s[18:19] sc1 nt
	s_add_u32 s18, s14, 0xa000
	s_addc_u32 s19, s15, 0
	global_load_dwordx4 v[20:23], v208, s[18:19] sc1 nt
	s_add_u32 s18, s14, 0xc000
	s_addc_u32 s19, s15, 0
	global_load_dwordx4 v[24:27], v208, s[18:19] sc1 nt
	s_add_u32 s18, s14, 0xe000
	s_addc_u32 s19, s15, 0
	global_load_dwordx4 v[28:31], v208, s[18:19] sc1 nt
	s_add_u32 s18, s14, 0x10000
	s_addc_u32 s19, s15, 0
	global_load_dwordx4 v[32:35], v208, s[18:19] sc1 nt
	s_add_u32 s18, s14, 0x12000
	s_addc_u32 s19, s15, 0
	global_load_dwordx4 v[36:39], v208, s[18:19] sc1 nt
	s_add_u32 s18, s14, 0x14000
	s_addc_u32 s19, s15, 0
	global_load_dwordx4 v[40:43], v208, s[18:19] sc1 nt
	s_add_u32 s18, s14, 0x16000
	s_addc_u32 s19, s15, 0
	global_load_dwordx4 v[44:47], v208, s[18:19] sc1 nt
	s_add_u32 s18, s14, 0x18000
	s_addc_u32 s19, s15, 0
	global_load_dwordx4 v[48:51], v208, s[18:19] sc1 nt
	s_add_u32 s18, s14, 0x1a000
	s_addc_u32 s19, s15, 0
	global_load_dwordx4 v[52:55], v208, s[18:19] sc1 nt
	s_add_u32 s18, s14, 0x1c000
	s_addc_u32 s19, s15, 0
	global_load_dwordx4 v[56:59], v208, s[18:19] sc1 nt
	s_add_u32 s18, s14, 0x1e000
	s_addc_u32 s19, s15, 0
	global_load_dwordx4 v[60:63], v208, s[18:19] sc1 nt
	s_waitcnt vmcnt(40)
	s_add_i32 s1, s20, 16
	s_lshr_b32 s2, s1, 10
	s_and_b32 s4, s1, 0x3ff
	s_lshr_b32 s5, s4, 6
	s_and_b32 s4, s4, 63
	s_lshl_b32 s12, s2, 22
	s_lshl_b32 s13, s4, 16
	s_add_i32 s12, s12, s13
	s_lshl_b32 s13, s5, 7
	s_add_i32 s12, s12, s13
	s_add_u32 s24, s90, s12
	s_addc_u32 s25, s91, 0
	s_add_u32 s24, s24, 0x3b100000
	s_addc_u32 s25, s25, 0
	s_add_u32 s26, s24, 0x1000
	s_addc_u32 s27, s25, 0
	v_pk_mul_f32 v[64:65], v[64:65], s[16:17] op_sel_hi:[1,0]
	v_pk_mul_f32 v[66:67], v[66:67], s[16:17] op_sel_hi:[1,0]
	v_pk_mul_f32 v[68:69], v[68:69], s[16:17] op_sel_hi:[1,0]
	v_pk_mul_f32 v[70:71], v[70:71], s[16:17] op_sel_hi:[1,0]
	v_pk_mul_f32 v[72:73], v[72:73], s[16:17] op_sel_hi:[1,0]
	v_pk_mul_f32 v[74:75], v[74:75], s[16:17] op_sel_hi:[1,0]
	v_pk_mul_f32 v[76:77], v[76:77], s[16:17] op_sel_hi:[1,0]
	v_pk_mul_f32 v[78:79], v[78:79], s[16:17] op_sel_hi:[1,0]
	v_pk_mul_f32 v[80:81], v[80:81], s[16:17] op_sel_hi:[1,0]
	v_pk_mul_f32 v[82:83], v[82:83], s[16:17] op_sel_hi:[1,0]
	v_pk_mul_f32 v[84:85], v[84:85], s[16:17] op_sel_hi:[1,0]
	v_pk_mul_f32 v[86:87], v[86:87], s[16:17] op_sel_hi:[1,0]
	v_pk_mul_f32 v[88:89], v[88:89], s[16:17] op_sel_hi:[1,0]
	v_pk_mul_f32 v[90:91], v[90:91], s[16:17] op_sel_hi:[1,0]
	v_pk_mul_f32 v[92:93], v[92:93], s[16:17] op_sel_hi:[1,0]
	v_pk_mul_f32 v[94:95], v[94:95], s[16:17] op_sel_hi:[1,0]
	v_pk_mul_f32 v[96:97], v[96:97], s[16:17] op_sel_hi:[1,0]
	v_pk_mul_f32 v[98:99], v[98:99], s[16:17] op_sel_hi:[1,0]
	v_pk_mul_f32 v[100:101], v[100:101], s[16:17] op_sel_hi:[1,0]
	v_pk_mul_f32 v[102:103], v[102:103], s[16:17] op_sel_hi:[1,0]
	v_pk_mul_f32 v[104:105], v[104:105], s[16:17] op_sel_hi:[1,0]
	v_pk_mul_f32 v[106:107], v[106:107], s[16:17] op_sel_hi:[1,0]
	v_pk_mul_f32 v[108:109], v[108:109], s[16:17] op_sel_hi:[1,0]
	v_pk_mul_f32 v[110:111], v[110:111], s[16:17] op_sel_hi:[1,0]
	v_pk_mul_f32 v[112:113], v[112:113], s[16:17] op_sel_hi:[1,0]
	v_pk_mul_f32 v[114:115], v[114:115], s[16:17] op_sel_hi:[1,0]
	v_pk_mul_f32 v[116:117], v[116:117], s[16:17] op_sel_hi:[1,0]
	v_pk_mul_f32 v[118:119], v[118:119], s[16:17] op_sel_hi:[1,0]
	v_pk_mul_f32 v[120:121], v[120:121], s[16:17] op_sel_hi:[1,0]
	v_pk_mul_f32 v[122:123], v[122:123], s[16:17] op_sel_hi:[1,0]
	v_pk_mul_f32 v[124:125], v[124:125], s[16:17] op_sel_hi:[1,0]
	v_pk_mul_f32 v[126:127], v[126:127], s[16:17] op_sel_hi:[1,0]
	v_cvt_pk_fp8_f32 v192, v64, v68
	v_cvt_pk_fp8_f32 v192, v72, v76 op_sel:[0,0,1]
	v_cvt_pk_fp8_f32 v193, v80, v84
	v_cvt_pk_fp8_f32 v193, v88, v92 op_sel:[0,0,1]
	v_cvt_pk_fp8_f32 v194, v96, v100
	v_cvt_pk_fp8_f32 v194, v104, v108 op_sel:[0,0,1]
	v_cvt_pk_fp8_f32 v195, v112, v116
	v_cvt_pk_fp8_f32 v195, v120, v124 op_sel:[0,0,1]
	global_store_dwordx4 v209, v[192:195], s[24:25] sc1
	v_cvt_pk_fp8_f32 v196, v65, v69
	v_cvt_pk_fp8_f32 v196, v73, v77 op_sel:[0,0,1]
	v_cvt_pk_fp8_f32 v197, v81, v85
	v_cvt_pk_fp8_f32 v197, v89, v93 op_sel:[0,0,1]
	v_cvt_pk_fp8_f32 v198, v97, v101
	v_cvt_pk_fp8_f32 v198, v105, v109 op_sel:[0,0,1]
	v_cvt_pk_fp8_f32 v199, v113, v117
	v_cvt_pk_fp8_f32 v199, v121, v125 op_sel:[0,0,1]
	global_store_dwordx4 v209, v[196:199], s[24:25] offset:2048 sc1
	v_cvt_pk_fp8_f32 v200, v66, v70
	v_cvt_pk_fp8_f32 v200, v74, v78 op_sel:[0,0,1]
	v_cvt_pk_fp8_f32 v201, v82, v86
	v_cvt_pk_fp8_f32 v201, v90, v94 op_sel:[0,0,1]
	v_cvt_pk_fp8_f32 v202, v98, v102
	v_cvt_pk_fp8_f32 v202, v106, v110 op_sel:[0,0,1]
	v_cvt_pk_fp8_f32 v203, v114, v118
	v_cvt_pk_fp8_f32 v203, v122, v126 op_sel:[0,0,1]
	global_store_dwordx4 v209, v[200:203], s[26:27] sc1
	v_cvt_pk_fp8_f32 v204, v67, v71
	v_cvt_pk_fp8_f32 v204, v75, v79 op_sel:[0,0,1]
	v_cvt_pk_fp8_f32 v205, v83, v87
	v_cvt_pk_fp8_f32 v205, v91, v95 op_sel:[0,0,1]
	v_cvt_pk_fp8_f32 v206, v99, v103
	v_cvt_pk_fp8_f32 v206, v107, v111 op_sel:[0,0,1]
	v_cvt_pk_fp8_f32 v207, v115, v119
	v_cvt_pk_fp8_f32 v207, v123, v127 op_sel:[0,0,1]
	global_store_dwordx4 v209, v[204:207], s[26:27] offset:2048 sc1
	s_add_i32 s1, s20, 28
	s_lshr_b32 s2, s1, 10
	s_and_b32 s4, s1, 0x3ff
	s_lshr_b32 s5, s4, 6
	s_and_b32 s4, s4, 63
	s_lshl_b32 s12, s2, 24
	s_lshl_b32 s13, s5, 20
	s_add_i32 s12, s12, s13
	s_lshl_b32 s13, s4, 7
	s_add_i32 s12, s12, s13
	s_add_u32 s14, s70, s12
	s_addc_u32 s15, s71, 0
	global_load_dwordx4 v[64:67], v208, s[14:15] sc1 nt
	s_add_u32 s18, s14, 0x2000
	s_addc_u32 s19, s15, 0
	global_load_dwordx4 v[68:71], v208, s[18:19] sc1 nt
	s_add_u32 s18, s14, 0x4000
	s_addc_u32 s19, s15, 0
	global_load_dwordx4 v[72:75], v208, s[18:19] sc1 nt
	s_add_u32 s18, s14, 0x6000
	s_addc_u32 s19, s15, 0
	global_load_dwordx4 v[76:79], v208, s[18:19] sc1 nt
	s_add_u32 s18, s14, 0x8000
	s_addc_u32 s19, s15, 0
	global_load_dwordx4 v[80:83], v208, s[18:19] sc1 nt
	s_add_u32 s18, s14, 0xa000
	s_addc_u32 s19, s15, 0
	global_load_dwordx4 v[84:87], v208, s[18:19] sc1 nt
	s_add_u32 s18, s14, 0xc000
	s_addc_u32 s19, s15, 0
	global_load_dwordx4 v[88:91], v208, s[18:19] sc1 nt
	s_add_u32 s18, s14, 0xe000
	s_addc_u32 s19, s15, 0
	global_load_dwordx4 v[92:95], v208, s[18:19] sc1 nt
	s_add_u32 s18, s14, 0x10000
	s_addc_u32 s19, s15, 0
	global_load_dwordx4 v[96:99], v208, s[18:19] sc1 nt
	s_add_u32 s18, s14, 0x12000
	s_addc_u32 s19, s15, 0
	global_load_dwordx4 v[100:103], v208, s[18:19] sc1 nt
	s_add_u32 s18, s14, 0x14000
	s_addc_u32 s19, s15, 0
	global_load_dwordx4 v[104:107], v208, s[18:19] sc1 nt
	s_add_u32 s18, s14, 0x16000
	s_addc_u32 s19, s15, 0
	global_load_dwordx4 v[108:111], v208, s[18:19] sc1 nt
	s_add_u32 s18, s14, 0x18000
	s_addc_u32 s19, s15, 0
	global_load_dwordx4 v[112:115], v208, s[18:19] sc1 nt
	s_add_u32 s18, s14, 0x1a000
	s_addc_u32 s19, s15, 0
	global_load_dwordx4 v[116:119], v208, s[18:19] sc1 nt
	s_add_u32 s18, s14, 0x1c000
	s_addc_u32 s19, s15, 0
	global_load_dwordx4 v[120:123], v208, s[18:19] sc1 nt
	s_add_u32 s18, s14, 0x1e000
	s_addc_u32 s19, s15, 0
	global_load_dwordx4 v[124:127], v208, s[18:19] sc1 nt
	s_waitcnt vmcnt(40)
	s_add_i32 s1, s20, 20
	s_lshr_b32 s2, s1, 10
	s_and_b32 s4, s1, 0x3ff
	s_lshr_b32 s5, s4, 6
	s_and_b32 s4, s4, 63
	s_lshl_b32 s12, s2, 22
	s_lshl_b32 s13, s4, 16
	s_add_i32 s12, s12, s13
	s_lshl_b32 s13, s5, 7
	s_add_i32 s12, s12, s13
	s_add_u32 s24, s90, s12
	s_addc_u32 s25, s91, 0
	s_add_u32 s24, s24, 0x3b100000
	s_addc_u32 s25, s25, 0
	s_add_u32 s26, s24, 0x1000
	s_addc_u32 s27, s25, 0
	v_pk_mul_f32 v[128:129], v[128:129], s[16:17] op_sel_hi:[1,0]
	v_pk_mul_f32 v[130:131], v[130:131], s[16:17] op_sel_hi:[1,0]
	v_pk_mul_f32 v[132:133], v[132:133], s[16:17] op_sel_hi:[1,0]
	v_pk_mul_f32 v[134:135], v[134:135], s[16:17] op_sel_hi:[1,0]
	v_pk_mul_f32 v[136:137], v[136:137], s[16:17] op_sel_hi:[1,0]
	v_pk_mul_f32 v[138:139], v[138:139], s[16:17] op_sel_hi:[1,0]
	v_pk_mul_f32 v[140:141], v[140:141], s[16:17] op_sel_hi:[1,0]
	v_pk_mul_f32 v[142:143], v[142:143], s[16:17] op_sel_hi:[1,0]
	v_pk_mul_f32 v[144:145], v[144:145], s[16:17] op_sel_hi:[1,0]
	v_pk_mul_f32 v[146:147], v[146:147], s[16:17] op_sel_hi:[1,0]
	v_pk_mul_f32 v[148:149], v[148:149], s[16:17] op_sel_hi:[1,0]
	v_pk_mul_f32 v[150:151], v[150:151], s[16:17] op_sel_hi:[1,0]
	v_pk_mul_f32 v[152:153], v[152:153], s[16:17] op_sel_hi:[1,0]
	v_pk_mul_f32 v[154:155], v[154:155], s[16:17] op_sel_hi:[1,0]
	v_pk_mul_f32 v[156:157], v[156:157], s[16:17] op_sel_hi:[1,0]
	v_pk_mul_f32 v[158:159], v[158:159], s[16:17] op_sel_hi:[1,0]
	v_pk_mul_f32 v[160:161], v[160:161], s[16:17] op_sel_hi:[1,0]
	v_pk_mul_f32 v[162:163], v[162:163], s[16:17] op_sel_hi:[1,0]
	v_pk_mul_f32 v[164:165], v[164:165], s[16:17] op_sel_hi:[1,0]
	v_pk_mul_f32 v[166:167], v[166:167], s[16:17] op_sel_hi:[1,0]
	v_pk_mul_f32 v[168:169], v[168:169], s[16:17] op_sel_hi:[1,0]
	v_pk_mul_f32 v[170:171], v[170:171], s[16:17] op_sel_hi:[1,0]
	v_pk_mul_f32 v[172:173], v[172:173], s[16:17] op_sel_hi:[1,0]
	v_pk_mul_f32 v[174:175], v[174:175], s[16:17] op_sel_hi:[1,0]
	v_pk_mul_f32 v[176:177], v[176:177], s[16:17] op_sel_hi:[1,0]
	v_pk_mul_f32 v[178:179], v[178:179], s[16:17] op_sel_hi:[1,0]
	v_pk_mul_f32 v[180:181], v[180:181], s[16:17] op_sel_hi:[1,0]
	v_pk_mul_f32 v[182:183], v[182:183], s[16:17] op_sel_hi:[1,0]
	v_pk_mul_f32 v[184:185], v[184:185], s[16:17] op_sel_hi:[1,0]
	v_pk_mul_f32 v[186:187], v[186:187], s[16:17] op_sel_hi:[1,0]
	v_pk_mul_f32 v[188:189], v[188:189], s[16:17] op_sel_hi:[1,0]
	v_pk_mul_f32 v[190:191], v[190:191], s[16:17] op_sel_hi:[1,0]
	v_cvt_pk_fp8_f32 v192, v128, v132
	v_cvt_pk_fp8_f32 v192, v136, v140 op_sel:[0,0,1]
	v_cvt_pk_fp8_f32 v193, v144, v148
	v_cvt_pk_fp8_f32 v193, v152, v156 op_sel:[0,0,1]
	v_cvt_pk_fp8_f32 v194, v160, v164
	v_cvt_pk_fp8_f32 v194, v168, v172 op_sel:[0,0,1]
	v_cvt_pk_fp8_f32 v195, v176, v180
	v_cvt_pk_fp8_f32 v195, v184, v188 op_sel:[0,0,1]
	global_store_dwordx4 v209, v[192:195], s[24:25] sc1
	v_cvt_pk_fp8_f32 v196, v129, v133
	v_cvt_pk_fp8_f32 v196, v137, v141 op_sel:[0,0,1]
	v_cvt_pk_fp8_f32 v197, v145, v149
	v_cvt_pk_fp8_f32 v197, v153, v157 op_sel:[0,0,1]
	v_cvt_pk_fp8_f32 v198, v161, v165
	v_cvt_pk_fp8_f32 v198, v169, v173 op_sel:[0,0,1]
	v_cvt_pk_fp8_f32 v199, v177, v181
	v_cvt_pk_fp8_f32 v199, v185, v189 op_sel:[0,0,1]
	global_store_dwordx4 v209, v[196:199], s[24:25] offset:2048 sc1
	v_cvt_pk_fp8_f32 v200, v130, v134
	v_cvt_pk_fp8_f32 v200, v138, v142 op_sel:[0,0,1]
	v_cvt_pk_fp8_f32 v201, v146, v150
	v_cvt_pk_fp8_f32 v201, v154, v158 op_sel:[0,0,1]
	v_cvt_pk_fp8_f32 v202, v162, v166
	v_cvt_pk_fp8_f32 v202, v170, v174 op_sel:[0,0,1]
	v_cvt_pk_fp8_f32 v203, v178, v182
	v_cvt_pk_fp8_f32 v203, v186, v190 op_sel:[0,0,1]
	global_store_dwordx4 v209, v[200:203], s[26:27] sc1
	v_cvt_pk_fp8_f32 v204, v131, v135
	v_cvt_pk_fp8_f32 v204, v139, v143 op_sel:[0,0,1]
	v_cvt_pk_fp8_f32 v205, v147, v151
	v_cvt_pk_fp8_f32 v205, v155, v159 op_sel:[0,0,1]
	v_cvt_pk_fp8_f32 v206, v163, v167
	v_cvt_pk_fp8_f32 v206, v171, v175 op_sel:[0,0,1]
	v_cvt_pk_fp8_f32 v207, v179, v183
	v_cvt_pk_fp8_f32 v207, v187, v191 op_sel:[0,0,1]
	global_store_dwordx4 v209, v[204:207], s[26:27] offset:2048 sc1
	s_add_i32 s1, s20, 32
	s_lshr_b32 s2, s1, 10
	s_and_b32 s4, s1, 0x3ff
	s_lshr_b32 s5, s4, 6
	s_and_b32 s4, s4, 63
	s_lshl_b32 s12, s2, 24
	s_lshl_b32 s13, s5, 20
	s_add_i32 s12, s12, s13
	s_lshl_b32 s13, s4, 7
	s_add_i32 s12, s12, s13
	s_add_u32 s14, s70, s12
	s_addc_u32 s15, s71, 0
	global_load_dwordx4 v[128:131], v208, s[14:15] sc1 nt
	s_add_u32 s18, s14, 0x2000
	s_addc_u32 s19, s15, 0
	global_load_dwordx4 v[132:135], v208, s[18:19] sc1 nt
	s_add_u32 s18, s14, 0x4000
	s_addc_u32 s19, s15, 0
	global_load_dwordx4 v[136:139], v208, s[18:19] sc1 nt
	s_add_u32 s18, s14, 0x6000
	s_addc_u32 s19, s15, 0
	global_load_dwordx4 v[140:143], v208, s[18:19] sc1 nt
	s_add_u32 s18, s14, 0x8000
	s_addc_u32 s19, s15, 0
	global_load_dwordx4 v[144:147], v208, s[18:19] sc1 nt
	s_add_u32 s18, s14, 0xa000
	s_addc_u32 s19, s15, 0
	global_load_dwordx4 v[148:151], v208, s[18:19] sc1 nt
	s_add_u32 s18, s14, 0xc000
	s_addc_u32 s19, s15, 0
	global_load_dwordx4 v[152:155], v208, s[18:19] sc1 nt
	s_add_u32 s18, s14, 0xe000
	s_addc_u32 s19, s15, 0
	global_load_dwordx4 v[156:159], v208, s[18:19] sc1 nt
	s_add_u32 s18, s14, 0x10000
	s_addc_u32 s19, s15, 0
	global_load_dwordx4 v[160:163], v208, s[18:19] sc1 nt
	s_add_u32 s18, s14, 0x12000
	s_addc_u32 s19, s15, 0
	global_load_dwordx4 v[164:167], v208, s[18:19] sc1 nt
	s_add_u32 s18, s14, 0x14000
	s_addc_u32 s19, s15, 0
	global_load_dwordx4 v[168:171], v208, s[18:19] sc1 nt
	s_add_u32 s18, s14, 0x16000
	s_addc_u32 s19, s15, 0
	global_load_dwordx4 v[172:175], v208, s[18:19] sc1 nt
	s_add_u32 s18, s14, 0x18000
	s_addc_u32 s19, s15, 0
	global_load_dwordx4 v[176:179], v208, s[18:19] sc1 nt
	s_add_u32 s18, s14, 0x1a000
	s_addc_u32 s19, s15, 0
	global_load_dwordx4 v[180:183], v208, s[18:19] sc1 nt
	s_add_u32 s18, s14, 0x1c000
	s_addc_u32 s19, s15, 0
	global_load_dwordx4 v[184:187], v208, s[18:19] sc1 nt
	s_add_u32 s18, s14, 0x1e000
	s_addc_u32 s19, s15, 0
	global_load_dwordx4 v[188:191], v208, s[18:19] sc1 nt
	s_waitcnt vmcnt(40)
	s_add_i32 s1, s20, 24
	s_lshr_b32 s2, s1, 10
	s_and_b32 s4, s1, 0x3ff
	s_lshr_b32 s5, s4, 6
	s_and_b32 s4, s4, 63
	s_lshl_b32 s12, s2, 22
	s_lshl_b32 s13, s4, 16
	s_add_i32 s12, s12, s13
	s_lshl_b32 s13, s5, 7
	s_add_i32 s12, s12, s13
	s_add_u32 s24, s90, s12
	s_addc_u32 s25, s91, 0
	s_add_u32 s24, s24, 0x3b100000
	s_addc_u32 s25, s25, 0
	s_add_u32 s26, s24, 0x1000
	s_addc_u32 s27, s25, 0
	v_pk_mul_f32 v[0:1], v[0:1], s[16:17] op_sel_hi:[1,0]
	v_pk_mul_f32 v[2:3], v[2:3], s[16:17] op_sel_hi:[1,0]
	v_pk_mul_f32 v[4:5], v[4:5], s[16:17] op_sel_hi:[1,0]
	v_pk_mul_f32 v[6:7], v[6:7], s[16:17] op_sel_hi:[1,0]
	v_pk_mul_f32 v[8:9], v[8:9], s[16:17] op_sel_hi:[1,0]
	v_pk_mul_f32 v[10:11], v[10:11], s[16:17] op_sel_hi:[1,0]
	v_pk_mul_f32 v[12:13], v[12:13], s[16:17] op_sel_hi:[1,0]
	v_pk_mul_f32 v[14:15], v[14:15], s[16:17] op_sel_hi:[1,0]
	v_pk_mul_f32 v[16:17], v[16:17], s[16:17] op_sel_hi:[1,0]
	v_pk_mul_f32 v[18:19], v[18:19], s[16:17] op_sel_hi:[1,0]
	v_pk_mul_f32 v[20:21], v[20:21], s[16:17] op_sel_hi:[1,0]
	v_pk_mul_f32 v[22:23], v[22:23], s[16:17] op_sel_hi:[1,0]
	v_pk_mul_f32 v[24:25], v[24:25], s[16:17] op_sel_hi:[1,0]
	v_pk_mul_f32 v[26:27], v[26:27], s[16:17] op_sel_hi:[1,0]
	v_pk_mul_f32 v[28:29], v[28:29], s[16:17] op_sel_hi:[1,0]
	v_pk_mul_f32 v[30:31], v[30:31], s[16:17] op_sel_hi:[1,0]
	v_pk_mul_f32 v[32:33], v[32:33], s[16:17] op_sel_hi:[1,0]
	v_pk_mul_f32 v[34:35], v[34:35], s[16:17] op_sel_hi:[1,0]
	v_pk_mul_f32 v[36:37], v[36:37], s[16:17] op_sel_hi:[1,0]
	v_pk_mul_f32 v[38:39], v[38:39], s[16:17] op_sel_hi:[1,0]
	v_pk_mul_f32 v[40:41], v[40:41], s[16:17] op_sel_hi:[1,0]
	v_pk_mul_f32 v[42:43], v[42:43], s[16:17] op_sel_hi:[1,0]
	v_pk_mul_f32 v[44:45], v[44:45], s[16:17] op_sel_hi:[1,0]
	v_pk_mul_f32 v[46:47], v[46:47], s[16:17] op_sel_hi:[1,0]
	v_pk_mul_f32 v[48:49], v[48:49], s[16:17] op_sel_hi:[1,0]
	v_pk_mul_f32 v[50:51], v[50:51], s[16:17] op_sel_hi:[1,0]
	v_pk_mul_f32 v[52:53], v[52:53], s[16:17] op_sel_hi:[1,0]
	v_pk_mul_f32 v[54:55], v[54:55], s[16:17] op_sel_hi:[1,0]
	v_pk_mul_f32 v[56:57], v[56:57], s[16:17] op_sel_hi:[1,0]
	v_pk_mul_f32 v[58:59], v[58:59], s[16:17] op_sel_hi:[1,0]
	v_pk_mul_f32 v[60:61], v[60:61], s[16:17] op_sel_hi:[1,0]
	v_pk_mul_f32 v[62:63], v[62:63], s[16:17] op_sel_hi:[1,0]
	v_cvt_pk_fp8_f32 v192, v0, v4
	v_cvt_pk_fp8_f32 v192, v8, v12 op_sel:[0,0,1]
	v_cvt_pk_fp8_f32 v193, v16, v20
	v_cvt_pk_fp8_f32 v193, v24, v28 op_sel:[0,0,1]
	v_cvt_pk_fp8_f32 v194, v32, v36
	v_cvt_pk_fp8_f32 v194, v40, v44 op_sel:[0,0,1]
	v_cvt_pk_fp8_f32 v195, v48, v52
	v_cvt_pk_fp8_f32 v195, v56, v60 op_sel:[0,0,1]
	global_store_dwordx4 v209, v[192:195], s[24:25] sc1
	v_cvt_pk_fp8_f32 v196, v1, v5
	v_cvt_pk_fp8_f32 v196, v9, v13 op_sel:[0,0,1]
	v_cvt_pk_fp8_f32 v197, v17, v21
	v_cvt_pk_fp8_f32 v197, v25, v29 op_sel:[0,0,1]
	v_cvt_pk_fp8_f32 v198, v33, v37
	v_cvt_pk_fp8_f32 v198, v41, v45 op_sel:[0,0,1]
	v_cvt_pk_fp8_f32 v199, v49, v53
	v_cvt_pk_fp8_f32 v199, v57, v61 op_sel:[0,0,1]
	global_store_dwordx4 v209, v[196:199], s[24:25] offset:2048 sc1
	v_cvt_pk_fp8_f32 v200, v2, v6
	v_cvt_pk_fp8_f32 v200, v10, v14 op_sel:[0,0,1]
	v_cvt_pk_fp8_f32 v201, v18, v22
	v_cvt_pk_fp8_f32 v201, v26, v30 op_sel:[0,0,1]
	v_cvt_pk_fp8_f32 v202, v34, v38
	v_cvt_pk_fp8_f32 v202, v42, v46 op_sel:[0,0,1]
	v_cvt_pk_fp8_f32 v203, v50, v54
	v_cvt_pk_fp8_f32 v203, v58, v62 op_sel:[0,0,1]
	global_store_dwordx4 v209, v[200:203], s[26:27] sc1
	v_cvt_pk_fp8_f32 v204, v3, v7
	v_cvt_pk_fp8_f32 v204, v11, v15 op_sel:[0,0,1]
	v_cvt_pk_fp8_f32 v205, v19, v23
	v_cvt_pk_fp8_f32 v205, v27, v31 op_sel:[0,0,1]
	v_cvt_pk_fp8_f32 v206, v35, v39
	v_cvt_pk_fp8_f32 v206, v43, v47 op_sel:[0,0,1]
	v_cvt_pk_fp8_f32 v207, v51, v55
	v_cvt_pk_fp8_f32 v207, v59, v63 op_sel:[0,0,1]
	global_store_dwordx4 v209, v[204:207], s[26:27] offset:2048 sc1
	s_add_i32 s1, s20, 36
	s_lshr_b32 s2, s1, 10
	s_and_b32 s4, s1, 0x3ff
	s_lshr_b32 s5, s4, 6
	s_and_b32 s4, s4, 63
	s_lshl_b32 s12, s2, 24
	s_lshl_b32 s13, s5, 20
	s_add_i32 s12, s12, s13
	s_lshl_b32 s13, s4, 7
	s_add_i32 s12, s12, s13
	s_add_u32 s14, s70, s12
	s_addc_u32 s15, s71, 0
	global_load_dwordx4 v[0:3], v208, s[14:15] sc1 nt
	s_add_u32 s18, s14, 0x2000
	s_addc_u32 s19, s15, 0
	global_load_dwordx4 v[4:7], v208, s[18:19] sc1 nt
	s_add_u32 s18, s14, 0x4000
	s_addc_u32 s19, s15, 0
	global_load_dwordx4 v[8:11], v208, s[18:19] sc1 nt
	s_add_u32 s18, s14, 0x6000
	s_addc_u32 s19, s15, 0
	global_load_dwordx4 v[12:15], v208, s[18:19] sc1 nt
	s_add_u32 s18, s14, 0x8000
	s_addc_u32 s19, s15, 0
	global_load_dwordx4 v[16:19], v208, s[18:19] sc1 nt
	s_add_u32 s18, s14, 0xa000
	s_addc_u32 s19, s15, 0
	global_load_dwordx4 v[20:23], v208, s[18:19] sc1 nt
	s_add_u32 s18, s14, 0xc000
	s_addc_u32 s19, s15, 0
	global_load_dwordx4 v[24:27], v208, s[18:19] sc1 nt
	s_add_u32 s18, s14, 0xe000
	s_addc_u32 s19, s15, 0
	global_load_dwordx4 v[28:31], v208, s[18:19] sc1 nt
	s_add_u32 s18, s14, 0x10000
	s_addc_u32 s19, s15, 0
	global_load_dwordx4 v[32:35], v208, s[18:19] sc1 nt
	s_add_u32 s18, s14, 0x12000
	s_addc_u32 s19, s15, 0
	global_load_dwordx4 v[36:39], v208, s[18:19] sc1 nt
	s_add_u32 s18, s14, 0x14000
	s_addc_u32 s19, s15, 0
	global_load_dwordx4 v[40:43], v208, s[18:19] sc1 nt
	s_add_u32 s18, s14, 0x16000
	s_addc_u32 s19, s15, 0
	global_load_dwordx4 v[44:47], v208, s[18:19] sc1 nt
	s_add_u32 s18, s14, 0x18000
	s_addc_u32 s19, s15, 0
	global_load_dwordx4 v[48:51], v208, s[18:19] sc1 nt
	s_add_u32 s18, s14, 0x1a000
	s_addc_u32 s19, s15, 0
	global_load_dwordx4 v[52:55], v208, s[18:19] sc1 nt
	s_add_u32 s18, s14, 0x1c000
	s_addc_u32 s19, s15, 0
	global_load_dwordx4 v[56:59], v208, s[18:19] sc1 nt
	s_add_u32 s18, s14, 0x1e000
	s_addc_u32 s19, s15, 0
	global_load_dwordx4 v[60:63], v208, s[18:19] sc1 nt
	s_waitcnt vmcnt(40)
	s_add_i32 s1, s20, 28
	s_lshr_b32 s2, s1, 10
	s_and_b32 s4, s1, 0x3ff
	s_lshr_b32 s5, s4, 6
	s_and_b32 s4, s4, 63
	s_lshl_b32 s12, s2, 22
	s_lshl_b32 s13, s4, 16
	s_add_i32 s12, s12, s13
	s_lshl_b32 s13, s5, 7
	s_add_i32 s12, s12, s13
	s_add_u32 s24, s90, s12
	s_addc_u32 s25, s91, 0
	s_add_u32 s24, s24, 0x3b100000
	s_addc_u32 s25, s25, 0
	s_add_u32 s26, s24, 0x1000
	s_addc_u32 s27, s25, 0
	v_pk_mul_f32 v[64:65], v[64:65], s[16:17] op_sel_hi:[1,0]
	v_pk_mul_f32 v[66:67], v[66:67], s[16:17] op_sel_hi:[1,0]
	v_pk_mul_f32 v[68:69], v[68:69], s[16:17] op_sel_hi:[1,0]
	v_pk_mul_f32 v[70:71], v[70:71], s[16:17] op_sel_hi:[1,0]
	v_pk_mul_f32 v[72:73], v[72:73], s[16:17] op_sel_hi:[1,0]
	v_pk_mul_f32 v[74:75], v[74:75], s[16:17] op_sel_hi:[1,0]
	v_pk_mul_f32 v[76:77], v[76:77], s[16:17] op_sel_hi:[1,0]
	v_pk_mul_f32 v[78:79], v[78:79], s[16:17] op_sel_hi:[1,0]
	v_pk_mul_f32 v[80:81], v[80:81], s[16:17] op_sel_hi:[1,0]
	v_pk_mul_f32 v[82:83], v[82:83], s[16:17] op_sel_hi:[1,0]
	v_pk_mul_f32 v[84:85], v[84:85], s[16:17] op_sel_hi:[1,0]
	v_pk_mul_f32 v[86:87], v[86:87], s[16:17] op_sel_hi:[1,0]
	v_pk_mul_f32 v[88:89], v[88:89], s[16:17] op_sel_hi:[1,0]
	v_pk_mul_f32 v[90:91], v[90:91], s[16:17] op_sel_hi:[1,0]
	v_pk_mul_f32 v[92:93], v[92:93], s[16:17] op_sel_hi:[1,0]
	v_pk_mul_f32 v[94:95], v[94:95], s[16:17] op_sel_hi:[1,0]
	v_pk_mul_f32 v[96:97], v[96:97], s[16:17] op_sel_hi:[1,0]
	v_pk_mul_f32 v[98:99], v[98:99], s[16:17] op_sel_hi:[1,0]
	v_pk_mul_f32 v[100:101], v[100:101], s[16:17] op_sel_hi:[1,0]
	v_pk_mul_f32 v[102:103], v[102:103], s[16:17] op_sel_hi:[1,0]
	v_pk_mul_f32 v[104:105], v[104:105], s[16:17] op_sel_hi:[1,0]
	v_pk_mul_f32 v[106:107], v[106:107], s[16:17] op_sel_hi:[1,0]
	v_pk_mul_f32 v[108:109], v[108:109], s[16:17] op_sel_hi:[1,0]
	v_pk_mul_f32 v[110:111], v[110:111], s[16:17] op_sel_hi:[1,0]
	v_pk_mul_f32 v[112:113], v[112:113], s[16:17] op_sel_hi:[1,0]
	v_pk_mul_f32 v[114:115], v[114:115], s[16:17] op_sel_hi:[1,0]
	v_pk_mul_f32 v[116:117], v[116:117], s[16:17] op_sel_hi:[1,0]
	v_pk_mul_f32 v[118:119], v[118:119], s[16:17] op_sel_hi:[1,0]
	v_pk_mul_f32 v[120:121], v[120:121], s[16:17] op_sel_hi:[1,0]
	v_pk_mul_f32 v[122:123], v[122:123], s[16:17] op_sel_hi:[1,0]
	v_pk_mul_f32 v[124:125], v[124:125], s[16:17] op_sel_hi:[1,0]
	v_pk_mul_f32 v[126:127], v[126:127], s[16:17] op_sel_hi:[1,0]
	v_cvt_pk_fp8_f32 v192, v64, v68
	v_cvt_pk_fp8_f32 v192, v72, v76 op_sel:[0,0,1]
	v_cvt_pk_fp8_f32 v193, v80, v84
	v_cvt_pk_fp8_f32 v193, v88, v92 op_sel:[0,0,1]
	v_cvt_pk_fp8_f32 v194, v96, v100
	v_cvt_pk_fp8_f32 v194, v104, v108 op_sel:[0,0,1]
	v_cvt_pk_fp8_f32 v195, v112, v116
	v_cvt_pk_fp8_f32 v195, v120, v124 op_sel:[0,0,1]
	global_store_dwordx4 v209, v[192:195], s[24:25] sc1
	v_cvt_pk_fp8_f32 v196, v65, v69
	v_cvt_pk_fp8_f32 v196, v73, v77 op_sel:[0,0,1]
	v_cvt_pk_fp8_f32 v197, v81, v85
	v_cvt_pk_fp8_f32 v197, v89, v93 op_sel:[0,0,1]
	v_cvt_pk_fp8_f32 v198, v97, v101
	v_cvt_pk_fp8_f32 v198, v105, v109 op_sel:[0,0,1]
	v_cvt_pk_fp8_f32 v199, v113, v117
	v_cvt_pk_fp8_f32 v199, v121, v125 op_sel:[0,0,1]
	global_store_dwordx4 v209, v[196:199], s[24:25] offset:2048 sc1
	v_cvt_pk_fp8_f32 v200, v66, v70
	v_cvt_pk_fp8_f32 v200, v74, v78 op_sel:[0,0,1]
	v_cvt_pk_fp8_f32 v201, v82, v86
	v_cvt_pk_fp8_f32 v201, v90, v94 op_sel:[0,0,1]
	v_cvt_pk_fp8_f32 v202, v98, v102
	v_cvt_pk_fp8_f32 v202, v106, v110 op_sel:[0,0,1]
	v_cvt_pk_fp8_f32 v203, v114, v118
	v_cvt_pk_fp8_f32 v203, v122, v126 op_sel:[0,0,1]
	global_store_dwordx4 v209, v[200:203], s[26:27] sc1
	v_cvt_pk_fp8_f32 v204, v67, v71
	v_cvt_pk_fp8_f32 v204, v75, v79 op_sel:[0,0,1]
	v_cvt_pk_fp8_f32 v205, v83, v87
	v_cvt_pk_fp8_f32 v205, v91, v95 op_sel:[0,0,1]
	v_cvt_pk_fp8_f32 v206, v99, v103
	v_cvt_pk_fp8_f32 v206, v107, v111 op_sel:[0,0,1]
	v_cvt_pk_fp8_f32 v207, v115, v119
	v_cvt_pk_fp8_f32 v207, v123, v127 op_sel:[0,0,1]
	global_store_dwordx4 v209, v[204:207], s[26:27] offset:2048 sc1
	s_add_i32 s1, s20, 40
	s_lshr_b32 s2, s1, 10
	s_and_b32 s4, s1, 0x3ff
	s_lshr_b32 s5, s4, 6
	s_and_b32 s4, s4, 63
	s_lshl_b32 s12, s2, 24
	s_lshl_b32 s13, s5, 20
	s_add_i32 s12, s12, s13
	s_lshl_b32 s13, s4, 7
	s_add_i32 s12, s12, s13
	s_add_u32 s14, s70, s12
	s_addc_u32 s15, s71, 0
	global_load_dwordx4 v[64:67], v208, s[14:15] sc1 nt
	s_add_u32 s18, s14, 0x2000
	s_addc_u32 s19, s15, 0
	global_load_dwordx4 v[68:71], v208, s[18:19] sc1 nt
	s_add_u32 s18, s14, 0x4000
	s_addc_u32 s19, s15, 0
	global_load_dwordx4 v[72:75], v208, s[18:19] sc1 nt
	s_add_u32 s18, s14, 0x6000
	s_addc_u32 s19, s15, 0
	global_load_dwordx4 v[76:79], v208, s[18:19] sc1 nt
	s_add_u32 s18, s14, 0x8000
	s_addc_u32 s19, s15, 0
	global_load_dwordx4 v[80:83], v208, s[18:19] sc1 nt
	s_add_u32 s18, s14, 0xa000
	s_addc_u32 s19, s15, 0
	global_load_dwordx4 v[84:87], v208, s[18:19] sc1 nt
	s_add_u32 s18, s14, 0xc000
	s_addc_u32 s19, s15, 0
	global_load_dwordx4 v[88:91], v208, s[18:19] sc1 nt
	s_add_u32 s18, s14, 0xe000
	s_addc_u32 s19, s15, 0
	global_load_dwordx4 v[92:95], v208, s[18:19] sc1 nt
	s_add_u32 s18, s14, 0x10000
	s_addc_u32 s19, s15, 0
	global_load_dwordx4 v[96:99], v208, s[18:19] sc1 nt
	s_add_u32 s18, s14, 0x12000
	s_addc_u32 s19, s15, 0
	global_load_dwordx4 v[100:103], v208, s[18:19] sc1 nt
	s_add_u32 s18, s14, 0x14000
	s_addc_u32 s19, s15, 0
	global_load_dwordx4 v[104:107], v208, s[18:19] sc1 nt
	s_add_u32 s18, s14, 0x16000
	s_addc_u32 s19, s15, 0
	global_load_dwordx4 v[108:111], v208, s[18:19] sc1 nt
	s_add_u32 s18, s14, 0x18000
	s_addc_u32 s19, s15, 0
	global_load_dwordx4 v[112:115], v208, s[18:19] sc1 nt
	s_add_u32 s18, s14, 0x1a000
	s_addc_u32 s19, s15, 0
	global_load_dwordx4 v[116:119], v208, s[18:19] sc1 nt
	s_add_u32 s18, s14, 0x1c000
	s_addc_u32 s19, s15, 0
	global_load_dwordx4 v[120:123], v208, s[18:19] sc1 nt
	s_add_u32 s18, s14, 0x1e000
	s_addc_u32 s19, s15, 0
	global_load_dwordx4 v[124:127], v208, s[18:19] sc1 nt
	s_waitcnt vmcnt(40)
	s_add_i32 s1, s20, 32
	s_lshr_b32 s2, s1, 10
	s_and_b32 s4, s1, 0x3ff
	s_lshr_b32 s5, s4, 6
	s_and_b32 s4, s4, 63
	s_lshl_b32 s12, s2, 22
	s_lshl_b32 s13, s4, 16
	s_add_i32 s12, s12, s13
	s_lshl_b32 s13, s5, 7
	s_add_i32 s12, s12, s13
	s_add_u32 s24, s90, s12
	s_addc_u32 s25, s91, 0
	s_add_u32 s24, s24, 0x3b100000
	s_addc_u32 s25, s25, 0
	s_add_u32 s26, s24, 0x1000
	s_addc_u32 s27, s25, 0
	v_pk_mul_f32 v[128:129], v[128:129], s[16:17] op_sel_hi:[1,0]
	v_pk_mul_f32 v[130:131], v[130:131], s[16:17] op_sel_hi:[1,0]
	v_pk_mul_f32 v[132:133], v[132:133], s[16:17] op_sel_hi:[1,0]
	v_pk_mul_f32 v[134:135], v[134:135], s[16:17] op_sel_hi:[1,0]
	v_pk_mul_f32 v[136:137], v[136:137], s[16:17] op_sel_hi:[1,0]
	v_pk_mul_f32 v[138:139], v[138:139], s[16:17] op_sel_hi:[1,0]
	v_pk_mul_f32 v[140:141], v[140:141], s[16:17] op_sel_hi:[1,0]
	v_pk_mul_f32 v[142:143], v[142:143], s[16:17] op_sel_hi:[1,0]
	v_pk_mul_f32 v[144:145], v[144:145], s[16:17] op_sel_hi:[1,0]
	v_pk_mul_f32 v[146:147], v[146:147], s[16:17] op_sel_hi:[1,0]
	v_pk_mul_f32 v[148:149], v[148:149], s[16:17] op_sel_hi:[1,0]
	v_pk_mul_f32 v[150:151], v[150:151], s[16:17] op_sel_hi:[1,0]
	v_pk_mul_f32 v[152:153], v[152:153], s[16:17] op_sel_hi:[1,0]
	v_pk_mul_f32 v[154:155], v[154:155], s[16:17] op_sel_hi:[1,0]
	v_pk_mul_f32 v[156:157], v[156:157], s[16:17] op_sel_hi:[1,0]
	v_pk_mul_f32 v[158:159], v[158:159], s[16:17] op_sel_hi:[1,0]
	v_pk_mul_f32 v[160:161], v[160:161], s[16:17] op_sel_hi:[1,0]
	v_pk_mul_f32 v[162:163], v[162:163], s[16:17] op_sel_hi:[1,0]
	v_pk_mul_f32 v[164:165], v[164:165], s[16:17] op_sel_hi:[1,0]
	v_pk_mul_f32 v[166:167], v[166:167], s[16:17] op_sel_hi:[1,0]
	v_pk_mul_f32 v[168:169], v[168:169], s[16:17] op_sel_hi:[1,0]
	v_pk_mul_f32 v[170:171], v[170:171], s[16:17] op_sel_hi:[1,0]
	v_pk_mul_f32 v[172:173], v[172:173], s[16:17] op_sel_hi:[1,0]
	v_pk_mul_f32 v[174:175], v[174:175], s[16:17] op_sel_hi:[1,0]
	v_pk_mul_f32 v[176:177], v[176:177], s[16:17] op_sel_hi:[1,0]
	v_pk_mul_f32 v[178:179], v[178:179], s[16:17] op_sel_hi:[1,0]
	v_pk_mul_f32 v[180:181], v[180:181], s[16:17] op_sel_hi:[1,0]
	v_pk_mul_f32 v[182:183], v[182:183], s[16:17] op_sel_hi:[1,0]
	v_pk_mul_f32 v[184:185], v[184:185], s[16:17] op_sel_hi:[1,0]
	v_pk_mul_f32 v[186:187], v[186:187], s[16:17] op_sel_hi:[1,0]
	v_pk_mul_f32 v[188:189], v[188:189], s[16:17] op_sel_hi:[1,0]
	v_pk_mul_f32 v[190:191], v[190:191], s[16:17] op_sel_hi:[1,0]
	v_cvt_pk_fp8_f32 v192, v128, v132
	v_cvt_pk_fp8_f32 v192, v136, v140 op_sel:[0,0,1]
	v_cvt_pk_fp8_f32 v193, v144, v148
	v_cvt_pk_fp8_f32 v193, v152, v156 op_sel:[0,0,1]
	v_cvt_pk_fp8_f32 v194, v160, v164
	v_cvt_pk_fp8_f32 v194, v168, v172 op_sel:[0,0,1]
	v_cvt_pk_fp8_f32 v195, v176, v180
	v_cvt_pk_fp8_f32 v195, v184, v188 op_sel:[0,0,1]
	global_store_dwordx4 v209, v[192:195], s[24:25] sc1
	v_cvt_pk_fp8_f32 v196, v129, v133
	v_cvt_pk_fp8_f32 v196, v137, v141 op_sel:[0,0,1]
	v_cvt_pk_fp8_f32 v197, v145, v149
	v_cvt_pk_fp8_f32 v197, v153, v157 op_sel:[0,0,1]
	v_cvt_pk_fp8_f32 v198, v161, v165
	v_cvt_pk_fp8_f32 v198, v169, v173 op_sel:[0,0,1]
	v_cvt_pk_fp8_f32 v199, v177, v181
	v_cvt_pk_fp8_f32 v199, v185, v189 op_sel:[0,0,1]
	global_store_dwordx4 v209, v[196:199], s[24:25] offset:2048 sc1
	v_cvt_pk_fp8_f32 v200, v130, v134
	v_cvt_pk_fp8_f32 v200, v138, v142 op_sel:[0,0,1]
	v_cvt_pk_fp8_f32 v201, v146, v150
	v_cvt_pk_fp8_f32 v201, v154, v158 op_sel:[0,0,1]
	v_cvt_pk_fp8_f32 v202, v162, v166
	v_cvt_pk_fp8_f32 v202, v170, v174 op_sel:[0,0,1]
	v_cvt_pk_fp8_f32 v203, v178, v182
	v_cvt_pk_fp8_f32 v203, v186, v190 op_sel:[0,0,1]
	global_store_dwordx4 v209, v[200:203], s[26:27] sc1
	v_cvt_pk_fp8_f32 v204, v131, v135
	v_cvt_pk_fp8_f32 v204, v139, v143 op_sel:[0,0,1]
	v_cvt_pk_fp8_f32 v205, v147, v151
	v_cvt_pk_fp8_f32 v205, v155, v159 op_sel:[0,0,1]
	v_cvt_pk_fp8_f32 v206, v163, v167
	v_cvt_pk_fp8_f32 v206, v171, v175 op_sel:[0,0,1]
	v_cvt_pk_fp8_f32 v207, v179, v183
	v_cvt_pk_fp8_f32 v207, v187, v191 op_sel:[0,0,1]
	global_store_dwordx4 v209, v[204:207], s[26:27] offset:2048 sc1
	s_add_i32 s1, s20, 44
	s_lshr_b32 s2, s1, 10
	s_and_b32 s4, s1, 0x3ff
	s_lshr_b32 s5, s4, 6
	s_and_b32 s4, s4, 63
	s_lshl_b32 s12, s2, 24
	s_lshl_b32 s13, s5, 20
	s_add_i32 s12, s12, s13
	s_lshl_b32 s13, s4, 7
	s_add_i32 s12, s12, s13
	s_add_u32 s14, s70, s12
	s_addc_u32 s15, s71, 0
	global_load_dwordx4 v[128:131], v208, s[14:15] sc1 nt
	s_add_u32 s18, s14, 0x2000
	s_addc_u32 s19, s15, 0
	global_load_dwordx4 v[132:135], v208, s[18:19] sc1 nt
	s_add_u32 s18, s14, 0x4000
	s_addc_u32 s19, s15, 0
	global_load_dwordx4 v[136:139], v208, s[18:19] sc1 nt
	s_add_u32 s18, s14, 0x6000
	s_addc_u32 s19, s15, 0
	global_load_dwordx4 v[140:143], v208, s[18:19] sc1 nt
	s_add_u32 s18, s14, 0x8000
	s_addc_u32 s19, s15, 0
	global_load_dwordx4 v[144:147], v208, s[18:19] sc1 nt
	s_add_u32 s18, s14, 0xa000
	s_addc_u32 s19, s15, 0
	global_load_dwordx4 v[148:151], v208, s[18:19] sc1 nt
	s_add_u32 s18, s14, 0xc000
	s_addc_u32 s19, s15, 0
	global_load_dwordx4 v[152:155], v208, s[18:19] sc1 nt
	s_add_u32 s18, s14, 0xe000
	s_addc_u32 s19, s15, 0
	global_load_dwordx4 v[156:159], v208, s[18:19] sc1 nt
	s_add_u32 s18, s14, 0x10000
	s_addc_u32 s19, s15, 0
	global_load_dwordx4 v[160:163], v208, s[18:19] sc1 nt
	s_add_u32 s18, s14, 0x12000
	s_addc_u32 s19, s15, 0
	global_load_dwordx4 v[164:167], v208, s[18:19] sc1 nt
	s_add_u32 s18, s14, 0x14000
	s_addc_u32 s19, s15, 0
	global_load_dwordx4 v[168:171], v208, s[18:19] sc1 nt
	s_add_u32 s18, s14, 0x16000
	s_addc_u32 s19, s15, 0
	global_load_dwordx4 v[172:175], v208, s[18:19] sc1 nt
	s_add_u32 s18, s14, 0x18000
	s_addc_u32 s19, s15, 0
	global_load_dwordx4 v[176:179], v208, s[18:19] sc1 nt
	s_add_u32 s18, s14, 0x1a000
	s_addc_u32 s19, s15, 0
	global_load_dwordx4 v[180:183], v208, s[18:19] sc1 nt
	s_add_u32 s18, s14, 0x1c000
	s_addc_u32 s19, s15, 0
	global_load_dwordx4 v[184:187], v208, s[18:19] sc1 nt
	s_add_u32 s18, s14, 0x1e000
	s_addc_u32 s19, s15, 0
	global_load_dwordx4 v[188:191], v208, s[18:19] sc1 nt
	s_waitcnt vmcnt(40)
	s_add_i32 s1, s20, 36
	s_lshr_b32 s2, s1, 10
	s_and_b32 s4, s1, 0x3ff
	s_lshr_b32 s5, s4, 6
	s_and_b32 s4, s4, 63
	s_lshl_b32 s12, s2, 22
	s_lshl_b32 s13, s4, 16
	s_add_i32 s12, s12, s13
	s_lshl_b32 s13, s5, 7
	s_add_i32 s12, s12, s13
	s_add_u32 s24, s90, s12
	s_addc_u32 s25, s91, 0
	s_add_u32 s24, s24, 0x3b100000
	s_addc_u32 s25, s25, 0
	s_add_u32 s26, s24, 0x1000
	s_addc_u32 s27, s25, 0
	v_pk_mul_f32 v[0:1], v[0:1], s[16:17] op_sel_hi:[1,0]
	v_pk_mul_f32 v[2:3], v[2:3], s[16:17] op_sel_hi:[1,0]
	v_pk_mul_f32 v[4:5], v[4:5], s[16:17] op_sel_hi:[1,0]
	v_pk_mul_f32 v[6:7], v[6:7], s[16:17] op_sel_hi:[1,0]
	v_pk_mul_f32 v[8:9], v[8:9], s[16:17] op_sel_hi:[1,0]
	v_pk_mul_f32 v[10:11], v[10:11], s[16:17] op_sel_hi:[1,0]
	v_pk_mul_f32 v[12:13], v[12:13], s[16:17] op_sel_hi:[1,0]
	v_pk_mul_f32 v[14:15], v[14:15], s[16:17] op_sel_hi:[1,0]
	v_pk_mul_f32 v[16:17], v[16:17], s[16:17] op_sel_hi:[1,0]
	v_pk_mul_f32 v[18:19], v[18:19], s[16:17] op_sel_hi:[1,0]
	v_pk_mul_f32 v[20:21], v[20:21], s[16:17] op_sel_hi:[1,0]
	v_pk_mul_f32 v[22:23], v[22:23], s[16:17] op_sel_hi:[1,0]
	v_pk_mul_f32 v[24:25], v[24:25], s[16:17] op_sel_hi:[1,0]
	v_pk_mul_f32 v[26:27], v[26:27], s[16:17] op_sel_hi:[1,0]
	v_pk_mul_f32 v[28:29], v[28:29], s[16:17] op_sel_hi:[1,0]
	v_pk_mul_f32 v[30:31], v[30:31], s[16:17] op_sel_hi:[1,0]
	v_pk_mul_f32 v[32:33], v[32:33], s[16:17] op_sel_hi:[1,0]
	v_pk_mul_f32 v[34:35], v[34:35], s[16:17] op_sel_hi:[1,0]
	v_pk_mul_f32 v[36:37], v[36:37], s[16:17] op_sel_hi:[1,0]
	v_pk_mul_f32 v[38:39], v[38:39], s[16:17] op_sel_hi:[1,0]
	v_pk_mul_f32 v[40:41], v[40:41], s[16:17] op_sel_hi:[1,0]
	v_pk_mul_f32 v[42:43], v[42:43], s[16:17] op_sel_hi:[1,0]
	v_pk_mul_f32 v[44:45], v[44:45], s[16:17] op_sel_hi:[1,0]
	v_pk_mul_f32 v[46:47], v[46:47], s[16:17] op_sel_hi:[1,0]
	v_pk_mul_f32 v[48:49], v[48:49], s[16:17] op_sel_hi:[1,0]
	v_pk_mul_f32 v[50:51], v[50:51], s[16:17] op_sel_hi:[1,0]
	v_pk_mul_f32 v[52:53], v[52:53], s[16:17] op_sel_hi:[1,0]
	v_pk_mul_f32 v[54:55], v[54:55], s[16:17] op_sel_hi:[1,0]
	v_pk_mul_f32 v[56:57], v[56:57], s[16:17] op_sel_hi:[1,0]
	v_pk_mul_f32 v[58:59], v[58:59], s[16:17] op_sel_hi:[1,0]
	v_pk_mul_f32 v[60:61], v[60:61], s[16:17] op_sel_hi:[1,0]
	v_pk_mul_f32 v[62:63], v[62:63], s[16:17] op_sel_hi:[1,0]
	v_cvt_pk_fp8_f32 v192, v0, v4
	v_cvt_pk_fp8_f32 v192, v8, v12 op_sel:[0,0,1]
	v_cvt_pk_fp8_f32 v193, v16, v20
	v_cvt_pk_fp8_f32 v193, v24, v28 op_sel:[0,0,1]
	v_cvt_pk_fp8_f32 v194, v32, v36
	v_cvt_pk_fp8_f32 v194, v40, v44 op_sel:[0,0,1]
	v_cvt_pk_fp8_f32 v195, v48, v52
	v_cvt_pk_fp8_f32 v195, v56, v60 op_sel:[0,0,1]
	global_store_dwordx4 v209, v[192:195], s[24:25] sc1
	v_cvt_pk_fp8_f32 v196, v1, v5
	v_cvt_pk_fp8_f32 v196, v9, v13 op_sel:[0,0,1]
	v_cvt_pk_fp8_f32 v197, v17, v21
	v_cvt_pk_fp8_f32 v197, v25, v29 op_sel:[0,0,1]
	v_cvt_pk_fp8_f32 v198, v33, v37
	v_cvt_pk_fp8_f32 v198, v41, v45 op_sel:[0,0,1]
	v_cvt_pk_fp8_f32 v199, v49, v53
	v_cvt_pk_fp8_f32 v199, v57, v61 op_sel:[0,0,1]
	global_store_dwordx4 v209, v[196:199], s[24:25] offset:2048 sc1
	v_cvt_pk_fp8_f32 v200, v2, v6
	v_cvt_pk_fp8_f32 v200, v10, v14 op_sel:[0,0,1]
	v_cvt_pk_fp8_f32 v201, v18, v22
	v_cvt_pk_fp8_f32 v201, v26, v30 op_sel:[0,0,1]
	v_cvt_pk_fp8_f32 v202, v34, v38
	v_cvt_pk_fp8_f32 v202, v42, v46 op_sel:[0,0,1]
	v_cvt_pk_fp8_f32 v203, v50, v54
	v_cvt_pk_fp8_f32 v203, v58, v62 op_sel:[0,0,1]
	global_store_dwordx4 v209, v[200:203], s[26:27] sc1
	v_cvt_pk_fp8_f32 v204, v3, v7
	v_cvt_pk_fp8_f32 v204, v11, v15 op_sel:[0,0,1]
	v_cvt_pk_fp8_f32 v205, v19, v23
	v_cvt_pk_fp8_f32 v205, v27, v31 op_sel:[0,0,1]
	v_cvt_pk_fp8_f32 v206, v35, v39
	v_cvt_pk_fp8_f32 v206, v43, v47 op_sel:[0,0,1]
	v_cvt_pk_fp8_f32 v207, v51, v55
	v_cvt_pk_fp8_f32 v207, v59, v63 op_sel:[0,0,1]
	global_store_dwordx4 v209, v[204:207], s[26:27] offset:2048 sc1
	s_add_i32 s1, s20, 48
	s_lshr_b32 s2, s1, 10
	s_and_b32 s4, s1, 0x3ff
	s_lshr_b32 s5, s4, 6
	s_and_b32 s4, s4, 63
	s_lshl_b32 s12, s2, 24
	s_lshl_b32 s13, s5, 20
	s_add_i32 s12, s12, s13
	s_lshl_b32 s13, s4, 7
	s_add_i32 s12, s12, s13
	s_add_u32 s14, s70, s12
	s_addc_u32 s15, s71, 0
	global_load_dwordx4 v[0:3], v208, s[14:15] sc1 nt
	s_add_u32 s18, s14, 0x2000
	s_addc_u32 s19, s15, 0
	global_load_dwordx4 v[4:7], v208, s[18:19] sc1 nt
	s_add_u32 s18, s14, 0x4000
	s_addc_u32 s19, s15, 0
	global_load_dwordx4 v[8:11], v208, s[18:19] sc1 nt
	s_add_u32 s18, s14, 0x6000
	s_addc_u32 s19, s15, 0
	global_load_dwordx4 v[12:15], v208, s[18:19] sc1 nt
	s_add_u32 s18, s14, 0x8000
	s_addc_u32 s19, s15, 0
	global_load_dwordx4 v[16:19], v208, s[18:19] sc1 nt
	s_add_u32 s18, s14, 0xa000
	s_addc_u32 s19, s15, 0
	global_load_dwordx4 v[20:23], v208, s[18:19] sc1 nt
	s_add_u32 s18, s14, 0xc000
	s_addc_u32 s19, s15, 0
	global_load_dwordx4 v[24:27], v208, s[18:19] sc1 nt
	s_add_u32 s18, s14, 0xe000
	s_addc_u32 s19, s15, 0
	global_load_dwordx4 v[28:31], v208, s[18:19] sc1 nt
	s_add_u32 s18, s14, 0x10000
	s_addc_u32 s19, s15, 0
	global_load_dwordx4 v[32:35], v208, s[18:19] sc1 nt
	s_add_u32 s18, s14, 0x12000
	s_addc_u32 s19, s15, 0
	global_load_dwordx4 v[36:39], v208, s[18:19] sc1 nt
	s_add_u32 s18, s14, 0x14000
	s_addc_u32 s19, s15, 0
	global_load_dwordx4 v[40:43], v208, s[18:19] sc1 nt
	s_add_u32 s18, s14, 0x16000
	s_addc_u32 s19, s15, 0
	global_load_dwordx4 v[44:47], v208, s[18:19] sc1 nt
	s_add_u32 s18, s14, 0x18000
	s_addc_u32 s19, s15, 0
	global_load_dwordx4 v[48:51], v208, s[18:19] sc1 nt
	s_add_u32 s18, s14, 0x1a000
	s_addc_u32 s19, s15, 0
	global_load_dwordx4 v[52:55], v208, s[18:19] sc1 nt
	s_add_u32 s18, s14, 0x1c000
	s_addc_u32 s19, s15, 0
	global_load_dwordx4 v[56:59], v208, s[18:19] sc1 nt
	s_add_u32 s18, s14, 0x1e000
	s_addc_u32 s19, s15, 0
	global_load_dwordx4 v[60:63], v208, s[18:19] sc1 nt
	s_waitcnt vmcnt(40)
	s_add_i32 s1, s20, 40
	s_lshr_b32 s2, s1, 10
	s_and_b32 s4, s1, 0x3ff
	s_lshr_b32 s5, s4, 6
	s_and_b32 s4, s4, 63
	s_lshl_b32 s12, s2, 22
	s_lshl_b32 s13, s4, 16
	s_add_i32 s12, s12, s13
	s_lshl_b32 s13, s5, 7
	s_add_i32 s12, s12, s13
	s_add_u32 s24, s90, s12
	s_addc_u32 s25, s91, 0
	s_add_u32 s24, s24, 0x3b100000
	s_addc_u32 s25, s25, 0
	s_add_u32 s26, s24, 0x1000
	s_addc_u32 s27, s25, 0
	v_pk_mul_f32 v[64:65], v[64:65], s[16:17] op_sel_hi:[1,0]
	v_pk_mul_f32 v[66:67], v[66:67], s[16:17] op_sel_hi:[1,0]
	v_pk_mul_f32 v[68:69], v[68:69], s[16:17] op_sel_hi:[1,0]
	v_pk_mul_f32 v[70:71], v[70:71], s[16:17] op_sel_hi:[1,0]
	v_pk_mul_f32 v[72:73], v[72:73], s[16:17] op_sel_hi:[1,0]
	v_pk_mul_f32 v[74:75], v[74:75], s[16:17] op_sel_hi:[1,0]
	v_pk_mul_f32 v[76:77], v[76:77], s[16:17] op_sel_hi:[1,0]
	v_pk_mul_f32 v[78:79], v[78:79], s[16:17] op_sel_hi:[1,0]
	v_pk_mul_f32 v[80:81], v[80:81], s[16:17] op_sel_hi:[1,0]
	v_pk_mul_f32 v[82:83], v[82:83], s[16:17] op_sel_hi:[1,0]
	v_pk_mul_f32 v[84:85], v[84:85], s[16:17] op_sel_hi:[1,0]
	v_pk_mul_f32 v[86:87], v[86:87], s[16:17] op_sel_hi:[1,0]
	v_pk_mul_f32 v[88:89], v[88:89], s[16:17] op_sel_hi:[1,0]
	v_pk_mul_f32 v[90:91], v[90:91], s[16:17] op_sel_hi:[1,0]
	v_pk_mul_f32 v[92:93], v[92:93], s[16:17] op_sel_hi:[1,0]
	v_pk_mul_f32 v[94:95], v[94:95], s[16:17] op_sel_hi:[1,0]
	v_pk_mul_f32 v[96:97], v[96:97], s[16:17] op_sel_hi:[1,0]
	v_pk_mul_f32 v[98:99], v[98:99], s[16:17] op_sel_hi:[1,0]
	v_pk_mul_f32 v[100:101], v[100:101], s[16:17] op_sel_hi:[1,0]
	v_pk_mul_f32 v[102:103], v[102:103], s[16:17] op_sel_hi:[1,0]
	v_pk_mul_f32 v[104:105], v[104:105], s[16:17] op_sel_hi:[1,0]
	v_pk_mul_f32 v[106:107], v[106:107], s[16:17] op_sel_hi:[1,0]
	v_pk_mul_f32 v[108:109], v[108:109], s[16:17] op_sel_hi:[1,0]
	v_pk_mul_f32 v[110:111], v[110:111], s[16:17] op_sel_hi:[1,0]
	v_pk_mul_f32 v[112:113], v[112:113], s[16:17] op_sel_hi:[1,0]
	v_pk_mul_f32 v[114:115], v[114:115], s[16:17] op_sel_hi:[1,0]
	v_pk_mul_f32 v[116:117], v[116:117], s[16:17] op_sel_hi:[1,0]
	v_pk_mul_f32 v[118:119], v[118:119], s[16:17] op_sel_hi:[1,0]
	v_pk_mul_f32 v[120:121], v[120:121], s[16:17] op_sel_hi:[1,0]
	v_pk_mul_f32 v[122:123], v[122:123], s[16:17] op_sel_hi:[1,0]
	v_pk_mul_f32 v[124:125], v[124:125], s[16:17] op_sel_hi:[1,0]
	v_pk_mul_f32 v[126:127], v[126:127], s[16:17] op_sel_hi:[1,0]
	v_cvt_pk_fp8_f32 v192, v64, v68
	v_cvt_pk_fp8_f32 v192, v72, v76 op_sel:[0,0,1]
	v_cvt_pk_fp8_f32 v193, v80, v84
	v_cvt_pk_fp8_f32 v193, v88, v92 op_sel:[0,0,1]
	v_cvt_pk_fp8_f32 v194, v96, v100
	v_cvt_pk_fp8_f32 v194, v104, v108 op_sel:[0,0,1]
	v_cvt_pk_fp8_f32 v195, v112, v116
	v_cvt_pk_fp8_f32 v195, v120, v124 op_sel:[0,0,1]
	global_store_dwordx4 v209, v[192:195], s[24:25] sc1
	v_cvt_pk_fp8_f32 v196, v65, v69
	v_cvt_pk_fp8_f32 v196, v73, v77 op_sel:[0,0,1]
	v_cvt_pk_fp8_f32 v197, v81, v85
	v_cvt_pk_fp8_f32 v197, v89, v93 op_sel:[0,0,1]
	v_cvt_pk_fp8_f32 v198, v97, v101
	v_cvt_pk_fp8_f32 v198, v105, v109 op_sel:[0,0,1]
	v_cvt_pk_fp8_f32 v199, v113, v117
	v_cvt_pk_fp8_f32 v199, v121, v125 op_sel:[0,0,1]
	global_store_dwordx4 v209, v[196:199], s[24:25] offset:2048 sc1
	v_cvt_pk_fp8_f32 v200, v66, v70
	v_cvt_pk_fp8_f32 v200, v74, v78 op_sel:[0,0,1]
	v_cvt_pk_fp8_f32 v201, v82, v86
	v_cvt_pk_fp8_f32 v201, v90, v94 op_sel:[0,0,1]
	v_cvt_pk_fp8_f32 v202, v98, v102
	v_cvt_pk_fp8_f32 v202, v106, v110 op_sel:[0,0,1]
	v_cvt_pk_fp8_f32 v203, v114, v118
	v_cvt_pk_fp8_f32 v203, v122, v126 op_sel:[0,0,1]
	global_store_dwordx4 v209, v[200:203], s[26:27] sc1
	v_cvt_pk_fp8_f32 v204, v67, v71
	v_cvt_pk_fp8_f32 v204, v75, v79 op_sel:[0,0,1]
	v_cvt_pk_fp8_f32 v205, v83, v87
	v_cvt_pk_fp8_f32 v205, v91, v95 op_sel:[0,0,1]
	v_cvt_pk_fp8_f32 v206, v99, v103
	v_cvt_pk_fp8_f32 v206, v107, v111 op_sel:[0,0,1]
	v_cvt_pk_fp8_f32 v207, v115, v119
	v_cvt_pk_fp8_f32 v207, v123, v127 op_sel:[0,0,1]
	global_store_dwordx4 v209, v[204:207], s[26:27] offset:2048 sc1
	s_add_i32 s1, s20, 52
	s_lshr_b32 s2, s1, 10
	s_and_b32 s4, s1, 0x3ff
	s_lshr_b32 s5, s4, 6
	s_and_b32 s4, s4, 63
	s_lshl_b32 s12, s2, 24
	s_lshl_b32 s13, s5, 20
	s_add_i32 s12, s12, s13
	s_lshl_b32 s13, s4, 7
	s_add_i32 s12, s12, s13
	s_add_u32 s14, s70, s12
	s_addc_u32 s15, s71, 0
	global_load_dwordx4 v[64:67], v208, s[14:15] sc1 nt
	s_add_u32 s18, s14, 0x2000
	s_addc_u32 s19, s15, 0
	global_load_dwordx4 v[68:71], v208, s[18:19] sc1 nt
	s_add_u32 s18, s14, 0x4000
	s_addc_u32 s19, s15, 0
	global_load_dwordx4 v[72:75], v208, s[18:19] sc1 nt
	s_add_u32 s18, s14, 0x6000
	s_addc_u32 s19, s15, 0
	global_load_dwordx4 v[76:79], v208, s[18:19] sc1 nt
	s_add_u32 s18, s14, 0x8000
	s_addc_u32 s19, s15, 0
	global_load_dwordx4 v[80:83], v208, s[18:19] sc1 nt
	s_add_u32 s18, s14, 0xa000
	s_addc_u32 s19, s15, 0
	global_load_dwordx4 v[84:87], v208, s[18:19] sc1 nt
	s_add_u32 s18, s14, 0xc000
	s_addc_u32 s19, s15, 0
	global_load_dwordx4 v[88:91], v208, s[18:19] sc1 nt
	s_add_u32 s18, s14, 0xe000
	s_addc_u32 s19, s15, 0
	global_load_dwordx4 v[92:95], v208, s[18:19] sc1 nt
	s_add_u32 s18, s14, 0x10000
	s_addc_u32 s19, s15, 0
	global_load_dwordx4 v[96:99], v208, s[18:19] sc1 nt
	s_add_u32 s18, s14, 0x12000
	s_addc_u32 s19, s15, 0
	global_load_dwordx4 v[100:103], v208, s[18:19] sc1 nt
	s_add_u32 s18, s14, 0x14000
	s_addc_u32 s19, s15, 0
	global_load_dwordx4 v[104:107], v208, s[18:19] sc1 nt
	s_add_u32 s18, s14, 0x16000
	s_addc_u32 s19, s15, 0
	global_load_dwordx4 v[108:111], v208, s[18:19] sc1 nt
	s_add_u32 s18, s14, 0x18000
	s_addc_u32 s19, s15, 0
	global_load_dwordx4 v[112:115], v208, s[18:19] sc1 nt
	s_add_u32 s18, s14, 0x1a000
	s_addc_u32 s19, s15, 0
	global_load_dwordx4 v[116:119], v208, s[18:19] sc1 nt
	s_add_u32 s18, s14, 0x1c000
	s_addc_u32 s19, s15, 0
	global_load_dwordx4 v[120:123], v208, s[18:19] sc1 nt
	s_add_u32 s18, s14, 0x1e000
	s_addc_u32 s19, s15, 0
	global_load_dwordx4 v[124:127], v208, s[18:19] sc1 nt
	s_waitcnt vmcnt(40)
	s_add_i32 s1, s20, 44
	s_lshr_b32 s2, s1, 10
	s_and_b32 s4, s1, 0x3ff
	s_lshr_b32 s5, s4, 6
	s_and_b32 s4, s4, 63
	s_lshl_b32 s12, s2, 22
	s_lshl_b32 s13, s4, 16
	s_add_i32 s12, s12, s13
	s_lshl_b32 s13, s5, 7
	s_add_i32 s12, s12, s13
	s_add_u32 s24, s90, s12
	s_addc_u32 s25, s91, 0
	s_add_u32 s24, s24, 0x3b100000
	s_addc_u32 s25, s25, 0
	s_add_u32 s26, s24, 0x1000
	s_addc_u32 s27, s25, 0
	v_pk_mul_f32 v[128:129], v[128:129], s[16:17] op_sel_hi:[1,0]
	v_pk_mul_f32 v[130:131], v[130:131], s[16:17] op_sel_hi:[1,0]
	v_pk_mul_f32 v[132:133], v[132:133], s[16:17] op_sel_hi:[1,0]
	v_pk_mul_f32 v[134:135], v[134:135], s[16:17] op_sel_hi:[1,0]
	v_pk_mul_f32 v[136:137], v[136:137], s[16:17] op_sel_hi:[1,0]
	v_pk_mul_f32 v[138:139], v[138:139], s[16:17] op_sel_hi:[1,0]
	v_pk_mul_f32 v[140:141], v[140:141], s[16:17] op_sel_hi:[1,0]
	v_pk_mul_f32 v[142:143], v[142:143], s[16:17] op_sel_hi:[1,0]
	v_pk_mul_f32 v[144:145], v[144:145], s[16:17] op_sel_hi:[1,0]
	v_pk_mul_f32 v[146:147], v[146:147], s[16:17] op_sel_hi:[1,0]
	v_pk_mul_f32 v[148:149], v[148:149], s[16:17] op_sel_hi:[1,0]
	v_pk_mul_f32 v[150:151], v[150:151], s[16:17] op_sel_hi:[1,0]
	v_pk_mul_f32 v[152:153], v[152:153], s[16:17] op_sel_hi:[1,0]
	v_pk_mul_f32 v[154:155], v[154:155], s[16:17] op_sel_hi:[1,0]
	v_pk_mul_f32 v[156:157], v[156:157], s[16:17] op_sel_hi:[1,0]
	v_pk_mul_f32 v[158:159], v[158:159], s[16:17] op_sel_hi:[1,0]
	v_pk_mul_f32 v[160:161], v[160:161], s[16:17] op_sel_hi:[1,0]
	v_pk_mul_f32 v[162:163], v[162:163], s[16:17] op_sel_hi:[1,0]
	v_pk_mul_f32 v[164:165], v[164:165], s[16:17] op_sel_hi:[1,0]
	v_pk_mul_f32 v[166:167], v[166:167], s[16:17] op_sel_hi:[1,0]
	v_pk_mul_f32 v[168:169], v[168:169], s[16:17] op_sel_hi:[1,0]
	v_pk_mul_f32 v[170:171], v[170:171], s[16:17] op_sel_hi:[1,0]
	v_pk_mul_f32 v[172:173], v[172:173], s[16:17] op_sel_hi:[1,0]
	v_pk_mul_f32 v[174:175], v[174:175], s[16:17] op_sel_hi:[1,0]
	v_pk_mul_f32 v[176:177], v[176:177], s[16:17] op_sel_hi:[1,0]
	v_pk_mul_f32 v[178:179], v[178:179], s[16:17] op_sel_hi:[1,0]
	v_pk_mul_f32 v[180:181], v[180:181], s[16:17] op_sel_hi:[1,0]
	v_pk_mul_f32 v[182:183], v[182:183], s[16:17] op_sel_hi:[1,0]
	v_pk_mul_f32 v[184:185], v[184:185], s[16:17] op_sel_hi:[1,0]
	v_pk_mul_f32 v[186:187], v[186:187], s[16:17] op_sel_hi:[1,0]
	v_pk_mul_f32 v[188:189], v[188:189], s[16:17] op_sel_hi:[1,0]
	v_pk_mul_f32 v[190:191], v[190:191], s[16:17] op_sel_hi:[1,0]
	v_cvt_pk_fp8_f32 v192, v128, v132
	v_cvt_pk_fp8_f32 v192, v136, v140 op_sel:[0,0,1]
	v_cvt_pk_fp8_f32 v193, v144, v148
	v_cvt_pk_fp8_f32 v193, v152, v156 op_sel:[0,0,1]
	v_cvt_pk_fp8_f32 v194, v160, v164
	v_cvt_pk_fp8_f32 v194, v168, v172 op_sel:[0,0,1]
	v_cvt_pk_fp8_f32 v195, v176, v180
	v_cvt_pk_fp8_f32 v195, v184, v188 op_sel:[0,0,1]
	global_store_dwordx4 v209, v[192:195], s[24:25] sc1
	v_cvt_pk_fp8_f32 v196, v129, v133
	v_cvt_pk_fp8_f32 v196, v137, v141 op_sel:[0,0,1]
	v_cvt_pk_fp8_f32 v197, v145, v149
	v_cvt_pk_fp8_f32 v197, v153, v157 op_sel:[0,0,1]
	v_cvt_pk_fp8_f32 v198, v161, v165
	v_cvt_pk_fp8_f32 v198, v169, v173 op_sel:[0,0,1]
	v_cvt_pk_fp8_f32 v199, v177, v181
	v_cvt_pk_fp8_f32 v199, v185, v189 op_sel:[0,0,1]
	global_store_dwordx4 v209, v[196:199], s[24:25] offset:2048 sc1
	v_cvt_pk_fp8_f32 v200, v130, v134
	v_cvt_pk_fp8_f32 v200, v138, v142 op_sel:[0,0,1]
	v_cvt_pk_fp8_f32 v201, v146, v150
	v_cvt_pk_fp8_f32 v201, v154, v158 op_sel:[0,0,1]
	v_cvt_pk_fp8_f32 v202, v162, v166
	v_cvt_pk_fp8_f32 v202, v170, v174 op_sel:[0,0,1]
	v_cvt_pk_fp8_f32 v203, v178, v182
	v_cvt_pk_fp8_f32 v203, v186, v190 op_sel:[0,0,1]
	global_store_dwordx4 v209, v[200:203], s[26:27] sc1
	v_cvt_pk_fp8_f32 v204, v131, v135
	v_cvt_pk_fp8_f32 v204, v139, v143 op_sel:[0,0,1]
	v_cvt_pk_fp8_f32 v205, v147, v151
	v_cvt_pk_fp8_f32 v205, v155, v159 op_sel:[0,0,1]
	v_cvt_pk_fp8_f32 v206, v163, v167
	v_cvt_pk_fp8_f32 v206, v171, v175 op_sel:[0,0,1]
	v_cvt_pk_fp8_f32 v207, v179, v183
	v_cvt_pk_fp8_f32 v207, v187, v191 op_sel:[0,0,1]
	global_store_dwordx4 v209, v[204:207], s[26:27] offset:2048 sc1
	s_add_i32 s1, s20, 56
	s_lshr_b32 s2, s1, 10
	s_and_b32 s4, s1, 0x3ff
	s_lshr_b32 s5, s4, 6
	s_and_b32 s4, s4, 63
	s_lshl_b32 s12, s2, 24
	s_lshl_b32 s13, s5, 20
	s_add_i32 s12, s12, s13
	s_lshl_b32 s13, s4, 7
	s_add_i32 s12, s12, s13
	s_add_u32 s14, s70, s12
	s_addc_u32 s15, s71, 0
	global_load_dwordx4 v[128:131], v208, s[14:15] sc1 nt
	s_add_u32 s18, s14, 0x2000
	s_addc_u32 s19, s15, 0
	global_load_dwordx4 v[132:135], v208, s[18:19] sc1 nt
	s_add_u32 s18, s14, 0x4000
	s_addc_u32 s19, s15, 0
	global_load_dwordx4 v[136:139], v208, s[18:19] sc1 nt
	s_add_u32 s18, s14, 0x6000
	s_addc_u32 s19, s15, 0
	global_load_dwordx4 v[140:143], v208, s[18:19] sc1 nt
	s_add_u32 s18, s14, 0x8000
	s_addc_u32 s19, s15, 0
	global_load_dwordx4 v[144:147], v208, s[18:19] sc1 nt
	s_add_u32 s18, s14, 0xa000
	s_addc_u32 s19, s15, 0
	global_load_dwordx4 v[148:151], v208, s[18:19] sc1 nt
	s_add_u32 s18, s14, 0xc000
	s_addc_u32 s19, s15, 0
	global_load_dwordx4 v[152:155], v208, s[18:19] sc1 nt
	s_add_u32 s18, s14, 0xe000
	s_addc_u32 s19, s15, 0
	global_load_dwordx4 v[156:159], v208, s[18:19] sc1 nt
	s_add_u32 s18, s14, 0x10000
	s_addc_u32 s19, s15, 0
	global_load_dwordx4 v[160:163], v208, s[18:19] sc1 nt
	s_add_u32 s18, s14, 0x12000
	s_addc_u32 s19, s15, 0
	global_load_dwordx4 v[164:167], v208, s[18:19] sc1 nt
	s_add_u32 s18, s14, 0x14000
	s_addc_u32 s19, s15, 0
	global_load_dwordx4 v[168:171], v208, s[18:19] sc1 nt
	s_add_u32 s18, s14, 0x16000
	s_addc_u32 s19, s15, 0
	global_load_dwordx4 v[172:175], v208, s[18:19] sc1 nt
	s_add_u32 s18, s14, 0x18000
	s_addc_u32 s19, s15, 0
	global_load_dwordx4 v[176:179], v208, s[18:19] sc1 nt
	s_add_u32 s18, s14, 0x1a000
	s_addc_u32 s19, s15, 0
	global_load_dwordx4 v[180:183], v208, s[18:19] sc1 nt
	s_add_u32 s18, s14, 0x1c000
	s_addc_u32 s19, s15, 0
	global_load_dwordx4 v[184:187], v208, s[18:19] sc1 nt
	s_add_u32 s18, s14, 0x1e000
	s_addc_u32 s19, s15, 0
	global_load_dwordx4 v[188:191], v208, s[18:19] sc1 nt
	s_waitcnt vmcnt(40)
	s_add_i32 s1, s20, 48
	s_lshr_b32 s2, s1, 10
	s_and_b32 s4, s1, 0x3ff
	s_lshr_b32 s5, s4, 6
	s_and_b32 s4, s4, 63
	s_lshl_b32 s12, s2, 22
	s_lshl_b32 s13, s4, 16
	s_add_i32 s12, s12, s13
	s_lshl_b32 s13, s5, 7
	s_add_i32 s12, s12, s13
	s_add_u32 s24, s90, s12
	s_addc_u32 s25, s91, 0
	s_add_u32 s24, s24, 0x3b100000
	s_addc_u32 s25, s25, 0
	s_add_u32 s26, s24, 0x1000
	s_addc_u32 s27, s25, 0
	v_pk_mul_f32 v[0:1], v[0:1], s[16:17] op_sel_hi:[1,0]
	v_pk_mul_f32 v[2:3], v[2:3], s[16:17] op_sel_hi:[1,0]
	v_pk_mul_f32 v[4:5], v[4:5], s[16:17] op_sel_hi:[1,0]
	v_pk_mul_f32 v[6:7], v[6:7], s[16:17] op_sel_hi:[1,0]
	v_pk_mul_f32 v[8:9], v[8:9], s[16:17] op_sel_hi:[1,0]
	v_pk_mul_f32 v[10:11], v[10:11], s[16:17] op_sel_hi:[1,0]
	v_pk_mul_f32 v[12:13], v[12:13], s[16:17] op_sel_hi:[1,0]
	v_pk_mul_f32 v[14:15], v[14:15], s[16:17] op_sel_hi:[1,0]
	v_pk_mul_f32 v[16:17], v[16:17], s[16:17] op_sel_hi:[1,0]
	v_pk_mul_f32 v[18:19], v[18:19], s[16:17] op_sel_hi:[1,0]
	v_pk_mul_f32 v[20:21], v[20:21], s[16:17] op_sel_hi:[1,0]
	v_pk_mul_f32 v[22:23], v[22:23], s[16:17] op_sel_hi:[1,0]
	v_pk_mul_f32 v[24:25], v[24:25], s[16:17] op_sel_hi:[1,0]
	v_pk_mul_f32 v[26:27], v[26:27], s[16:17] op_sel_hi:[1,0]
	v_pk_mul_f32 v[28:29], v[28:29], s[16:17] op_sel_hi:[1,0]
	v_pk_mul_f32 v[30:31], v[30:31], s[16:17] op_sel_hi:[1,0]
	v_pk_mul_f32 v[32:33], v[32:33], s[16:17] op_sel_hi:[1,0]
	v_pk_mul_f32 v[34:35], v[34:35], s[16:17] op_sel_hi:[1,0]
	v_pk_mul_f32 v[36:37], v[36:37], s[16:17] op_sel_hi:[1,0]
	v_pk_mul_f32 v[38:39], v[38:39], s[16:17] op_sel_hi:[1,0]
	v_pk_mul_f32 v[40:41], v[40:41], s[16:17] op_sel_hi:[1,0]
	v_pk_mul_f32 v[42:43], v[42:43], s[16:17] op_sel_hi:[1,0]
	v_pk_mul_f32 v[44:45], v[44:45], s[16:17] op_sel_hi:[1,0]
	v_pk_mul_f32 v[46:47], v[46:47], s[16:17] op_sel_hi:[1,0]
	v_pk_mul_f32 v[48:49], v[48:49], s[16:17] op_sel_hi:[1,0]
	v_pk_mul_f32 v[50:51], v[50:51], s[16:17] op_sel_hi:[1,0]
	v_pk_mul_f32 v[52:53], v[52:53], s[16:17] op_sel_hi:[1,0]
	v_pk_mul_f32 v[54:55], v[54:55], s[16:17] op_sel_hi:[1,0]
	v_pk_mul_f32 v[56:57], v[56:57], s[16:17] op_sel_hi:[1,0]
	v_pk_mul_f32 v[58:59], v[58:59], s[16:17] op_sel_hi:[1,0]
	v_pk_mul_f32 v[60:61], v[60:61], s[16:17] op_sel_hi:[1,0]
	v_pk_mul_f32 v[62:63], v[62:63], s[16:17] op_sel_hi:[1,0]
	v_cvt_pk_fp8_f32 v192, v0, v4
	v_cvt_pk_fp8_f32 v192, v8, v12 op_sel:[0,0,1]
	v_cvt_pk_fp8_f32 v193, v16, v20
	v_cvt_pk_fp8_f32 v193, v24, v28 op_sel:[0,0,1]
	v_cvt_pk_fp8_f32 v194, v32, v36
	v_cvt_pk_fp8_f32 v194, v40, v44 op_sel:[0,0,1]
	v_cvt_pk_fp8_f32 v195, v48, v52
	v_cvt_pk_fp8_f32 v195, v56, v60 op_sel:[0,0,1]
	global_store_dwordx4 v209, v[192:195], s[24:25] sc1
	v_cvt_pk_fp8_f32 v196, v1, v5
	v_cvt_pk_fp8_f32 v196, v9, v13 op_sel:[0,0,1]
	v_cvt_pk_fp8_f32 v197, v17, v21
	v_cvt_pk_fp8_f32 v197, v25, v29 op_sel:[0,0,1]
	v_cvt_pk_fp8_f32 v198, v33, v37
	v_cvt_pk_fp8_f32 v198, v41, v45 op_sel:[0,0,1]
	v_cvt_pk_fp8_f32 v199, v49, v53
	v_cvt_pk_fp8_f32 v199, v57, v61 op_sel:[0,0,1]
	global_store_dwordx4 v209, v[196:199], s[24:25] offset:2048 sc1
	v_cvt_pk_fp8_f32 v200, v2, v6
	v_cvt_pk_fp8_f32 v200, v10, v14 op_sel:[0,0,1]
	v_cvt_pk_fp8_f32 v201, v18, v22
	v_cvt_pk_fp8_f32 v201, v26, v30 op_sel:[0,0,1]
	v_cvt_pk_fp8_f32 v202, v34, v38
	v_cvt_pk_fp8_f32 v202, v42, v46 op_sel:[0,0,1]
	v_cvt_pk_fp8_f32 v203, v50, v54
	v_cvt_pk_fp8_f32 v203, v58, v62 op_sel:[0,0,1]
	global_store_dwordx4 v209, v[200:203], s[26:27] sc1
	v_cvt_pk_fp8_f32 v204, v3, v7
	v_cvt_pk_fp8_f32 v204, v11, v15 op_sel:[0,0,1]
	v_cvt_pk_fp8_f32 v205, v19, v23
	v_cvt_pk_fp8_f32 v205, v27, v31 op_sel:[0,0,1]
	v_cvt_pk_fp8_f32 v206, v35, v39
	v_cvt_pk_fp8_f32 v206, v43, v47 op_sel:[0,0,1]
	v_cvt_pk_fp8_f32 v207, v51, v55
	v_cvt_pk_fp8_f32 v207, v59, v63 op_sel:[0,0,1]
	global_store_dwordx4 v209, v[204:207], s[26:27] offset:2048 sc1
	s_add_i32 s1, s20, 60
	s_lshr_b32 s2, s1, 10
	s_and_b32 s4, s1, 0x3ff
	s_lshr_b32 s5, s4, 6
	s_and_b32 s4, s4, 63
	s_lshl_b32 s12, s2, 24
	s_lshl_b32 s13, s5, 20
	s_add_i32 s12, s12, s13
	s_lshl_b32 s13, s4, 7
	s_add_i32 s12, s12, s13
	s_add_u32 s14, s70, s12
	s_addc_u32 s15, s71, 0
	global_load_dwordx4 v[0:3], v208, s[14:15] sc1 nt
	s_add_u32 s18, s14, 0x2000
	s_addc_u32 s19, s15, 0
	global_load_dwordx4 v[4:7], v208, s[18:19] sc1 nt
	s_add_u32 s18, s14, 0x4000
	s_addc_u32 s19, s15, 0
	global_load_dwordx4 v[8:11], v208, s[18:19] sc1 nt
	s_add_u32 s18, s14, 0x6000
	s_addc_u32 s19, s15, 0
	global_load_dwordx4 v[12:15], v208, s[18:19] sc1 nt
	s_add_u32 s18, s14, 0x8000
	s_addc_u32 s19, s15, 0
	global_load_dwordx4 v[16:19], v208, s[18:19] sc1 nt
	s_add_u32 s18, s14, 0xa000
	s_addc_u32 s19, s15, 0
	global_load_dwordx4 v[20:23], v208, s[18:19] sc1 nt
	s_add_u32 s18, s14, 0xc000
	s_addc_u32 s19, s15, 0
	global_load_dwordx4 v[24:27], v208, s[18:19] sc1 nt
	s_add_u32 s18, s14, 0xe000
	s_addc_u32 s19, s15, 0
	global_load_dwordx4 v[28:31], v208, s[18:19] sc1 nt
	s_add_u32 s18, s14, 0x10000
	s_addc_u32 s19, s15, 0
	global_load_dwordx4 v[32:35], v208, s[18:19] sc1 nt
	s_add_u32 s18, s14, 0x12000
	s_addc_u32 s19, s15, 0
	global_load_dwordx4 v[36:39], v208, s[18:19] sc1 nt
	s_add_u32 s18, s14, 0x14000
	s_addc_u32 s19, s15, 0
	global_load_dwordx4 v[40:43], v208, s[18:19] sc1 nt
	s_add_u32 s18, s14, 0x16000
	s_addc_u32 s19, s15, 0
	global_load_dwordx4 v[44:47], v208, s[18:19] sc1 nt
	s_add_u32 s18, s14, 0x18000
	s_addc_u32 s19, s15, 0
	global_load_dwordx4 v[48:51], v208, s[18:19] sc1 nt
	s_add_u32 s18, s14, 0x1a000
	s_addc_u32 s19, s15, 0
	global_load_dwordx4 v[52:55], v208, s[18:19] sc1 nt
	s_add_u32 s18, s14, 0x1c000
	s_addc_u32 s19, s15, 0
	global_load_dwordx4 v[56:59], v208, s[18:19] sc1 nt
	s_add_u32 s18, s14, 0x1e000
	s_addc_u32 s19, s15, 0
	global_load_dwordx4 v[60:63], v208, s[18:19] sc1 nt
	s_waitcnt vmcnt(40)
	s_add_i32 s1, s20, 52
	s_lshr_b32 s2, s1, 10
	s_and_b32 s4, s1, 0x3ff
	s_lshr_b32 s5, s4, 6
	s_and_b32 s4, s4, 63
	s_lshl_b32 s12, s2, 22
	s_lshl_b32 s13, s4, 16
	s_add_i32 s12, s12, s13
	s_lshl_b32 s13, s5, 7
	s_add_i32 s12, s12, s13
	s_add_u32 s24, s90, s12
	s_addc_u32 s25, s91, 0
	s_add_u32 s24, s24, 0x3b100000
	s_addc_u32 s25, s25, 0
	s_add_u32 s26, s24, 0x1000
	s_addc_u32 s27, s25, 0
	v_pk_mul_f32 v[64:65], v[64:65], s[16:17] op_sel_hi:[1,0]
	v_pk_mul_f32 v[66:67], v[66:67], s[16:17] op_sel_hi:[1,0]
	v_pk_mul_f32 v[68:69], v[68:69], s[16:17] op_sel_hi:[1,0]
	v_pk_mul_f32 v[70:71], v[70:71], s[16:17] op_sel_hi:[1,0]
	v_pk_mul_f32 v[72:73], v[72:73], s[16:17] op_sel_hi:[1,0]
	v_pk_mul_f32 v[74:75], v[74:75], s[16:17] op_sel_hi:[1,0]
	v_pk_mul_f32 v[76:77], v[76:77], s[16:17] op_sel_hi:[1,0]
	v_pk_mul_f32 v[78:79], v[78:79], s[16:17] op_sel_hi:[1,0]
	v_pk_mul_f32 v[80:81], v[80:81], s[16:17] op_sel_hi:[1,0]
	v_pk_mul_f32 v[82:83], v[82:83], s[16:17] op_sel_hi:[1,0]
	v_pk_mul_f32 v[84:85], v[84:85], s[16:17] op_sel_hi:[1,0]
	v_pk_mul_f32 v[86:87], v[86:87], s[16:17] op_sel_hi:[1,0]
	v_pk_mul_f32 v[88:89], v[88:89], s[16:17] op_sel_hi:[1,0]
	v_pk_mul_f32 v[90:91], v[90:91], s[16:17] op_sel_hi:[1,0]
	v_pk_mul_f32 v[92:93], v[92:93], s[16:17] op_sel_hi:[1,0]
	v_pk_mul_f32 v[94:95], v[94:95], s[16:17] op_sel_hi:[1,0]
	v_pk_mul_f32 v[96:97], v[96:97], s[16:17] op_sel_hi:[1,0]
	v_pk_mul_f32 v[98:99], v[98:99], s[16:17] op_sel_hi:[1,0]
	v_pk_mul_f32 v[100:101], v[100:101], s[16:17] op_sel_hi:[1,0]
	v_pk_mul_f32 v[102:103], v[102:103], s[16:17] op_sel_hi:[1,0]
	v_pk_mul_f32 v[104:105], v[104:105], s[16:17] op_sel_hi:[1,0]
	v_pk_mul_f32 v[106:107], v[106:107], s[16:17] op_sel_hi:[1,0]
	v_pk_mul_f32 v[108:109], v[108:109], s[16:17] op_sel_hi:[1,0]
	v_pk_mul_f32 v[110:111], v[110:111], s[16:17] op_sel_hi:[1,0]
	v_pk_mul_f32 v[112:113], v[112:113], s[16:17] op_sel_hi:[1,0]
	v_pk_mul_f32 v[114:115], v[114:115], s[16:17] op_sel_hi:[1,0]
	v_pk_mul_f32 v[116:117], v[116:117], s[16:17] op_sel_hi:[1,0]
	v_pk_mul_f32 v[118:119], v[118:119], s[16:17] op_sel_hi:[1,0]
	v_pk_mul_f32 v[120:121], v[120:121], s[16:17] op_sel_hi:[1,0]
	v_pk_mul_f32 v[122:123], v[122:123], s[16:17] op_sel_hi:[1,0]
	v_pk_mul_f32 v[124:125], v[124:125], s[16:17] op_sel_hi:[1,0]
	v_pk_mul_f32 v[126:127], v[126:127], s[16:17] op_sel_hi:[1,0]
	v_cvt_pk_fp8_f32 v192, v64, v68
	v_cvt_pk_fp8_f32 v192, v72, v76 op_sel:[0,0,1]
	v_cvt_pk_fp8_f32 v193, v80, v84
	v_cvt_pk_fp8_f32 v193, v88, v92 op_sel:[0,0,1]
	v_cvt_pk_fp8_f32 v194, v96, v100
	v_cvt_pk_fp8_f32 v194, v104, v108 op_sel:[0,0,1]
	v_cvt_pk_fp8_f32 v195, v112, v116
	v_cvt_pk_fp8_f32 v195, v120, v124 op_sel:[0,0,1]
	global_store_dwordx4 v209, v[192:195], s[24:25] sc1
	v_cvt_pk_fp8_f32 v196, v65, v69
	v_cvt_pk_fp8_f32 v196, v73, v77 op_sel:[0,0,1]
	v_cvt_pk_fp8_f32 v197, v81, v85
	v_cvt_pk_fp8_f32 v197, v89, v93 op_sel:[0,0,1]
	v_cvt_pk_fp8_f32 v198, v97, v101
	v_cvt_pk_fp8_f32 v198, v105, v109 op_sel:[0,0,1]
	v_cvt_pk_fp8_f32 v199, v113, v117
	v_cvt_pk_fp8_f32 v199, v121, v125 op_sel:[0,0,1]
	global_store_dwordx4 v209, v[196:199], s[24:25] offset:2048 sc1
	v_cvt_pk_fp8_f32 v200, v66, v70
	v_cvt_pk_fp8_f32 v200, v74, v78 op_sel:[0,0,1]
	v_cvt_pk_fp8_f32 v201, v82, v86
	v_cvt_pk_fp8_f32 v201, v90, v94 op_sel:[0,0,1]
	v_cvt_pk_fp8_f32 v202, v98, v102
	v_cvt_pk_fp8_f32 v202, v106, v110 op_sel:[0,0,1]
	v_cvt_pk_fp8_f32 v203, v114, v118
	v_cvt_pk_fp8_f32 v203, v122, v126 op_sel:[0,0,1]
	global_store_dwordx4 v209, v[200:203], s[26:27] sc1
	v_cvt_pk_fp8_f32 v204, v67, v71
	v_cvt_pk_fp8_f32 v204, v75, v79 op_sel:[0,0,1]
	v_cvt_pk_fp8_f32 v205, v83, v87
	v_cvt_pk_fp8_f32 v205, v91, v95 op_sel:[0,0,1]
	v_cvt_pk_fp8_f32 v206, v99, v103
	v_cvt_pk_fp8_f32 v206, v107, v111 op_sel:[0,0,1]
	v_cvt_pk_fp8_f32 v207, v115, v119
	v_cvt_pk_fp8_f32 v207, v123, v127 op_sel:[0,0,1]
	global_store_dwordx4 v209, v[204:207], s[26:27] offset:2048 sc1
	s_waitcnt vmcnt(24)
	s_add_i32 s1, s20, 56
	s_lshr_b32 s2, s1, 10
	s_and_b32 s4, s1, 0x3ff
	s_lshr_b32 s5, s4, 6
	s_and_b32 s4, s4, 63
	s_lshl_b32 s12, s2, 22
	s_lshl_b32 s13, s4, 16
	s_add_i32 s12, s12, s13
	s_lshl_b32 s13, s5, 7
	s_add_i32 s12, s12, s13
	s_add_u32 s24, s90, s12
	s_addc_u32 s25, s91, 0
	s_add_u32 s24, s24, 0x3b100000
	s_addc_u32 s25, s25, 0
	s_add_u32 s26, s24, 0x1000
	s_addc_u32 s27, s25, 0
	v_pk_mul_f32 v[128:129], v[128:129], s[16:17] op_sel_hi:[1,0]
	v_pk_mul_f32 v[130:131], v[130:131], s[16:17] op_sel_hi:[1,0]
	v_pk_mul_f32 v[132:133], v[132:133], s[16:17] op_sel_hi:[1,0]
	v_pk_mul_f32 v[134:135], v[134:135], s[16:17] op_sel_hi:[1,0]
	v_pk_mul_f32 v[136:137], v[136:137], s[16:17] op_sel_hi:[1,0]
	v_pk_mul_f32 v[138:139], v[138:139], s[16:17] op_sel_hi:[1,0]
	v_pk_mul_f32 v[140:141], v[140:141], s[16:17] op_sel_hi:[1,0]
	v_pk_mul_f32 v[142:143], v[142:143], s[16:17] op_sel_hi:[1,0]
	v_pk_mul_f32 v[144:145], v[144:145], s[16:17] op_sel_hi:[1,0]
	v_pk_mul_f32 v[146:147], v[146:147], s[16:17] op_sel_hi:[1,0]
	v_pk_mul_f32 v[148:149], v[148:149], s[16:17] op_sel_hi:[1,0]
	v_pk_mul_f32 v[150:151], v[150:151], s[16:17] op_sel_hi:[1,0]
	v_pk_mul_f32 v[152:153], v[152:153], s[16:17] op_sel_hi:[1,0]
	v_pk_mul_f32 v[154:155], v[154:155], s[16:17] op_sel_hi:[1,0]
	v_pk_mul_f32 v[156:157], v[156:157], s[16:17] op_sel_hi:[1,0]
	v_pk_mul_f32 v[158:159], v[158:159], s[16:17] op_sel_hi:[1,0]
	v_pk_mul_f32 v[160:161], v[160:161], s[16:17] op_sel_hi:[1,0]
	v_pk_mul_f32 v[162:163], v[162:163], s[16:17] op_sel_hi:[1,0]
	v_pk_mul_f32 v[164:165], v[164:165], s[16:17] op_sel_hi:[1,0]
	v_pk_mul_f32 v[166:167], v[166:167], s[16:17] op_sel_hi:[1,0]
	v_pk_mul_f32 v[168:169], v[168:169], s[16:17] op_sel_hi:[1,0]
	v_pk_mul_f32 v[170:171], v[170:171], s[16:17] op_sel_hi:[1,0]
	v_pk_mul_f32 v[172:173], v[172:173], s[16:17] op_sel_hi:[1,0]
	v_pk_mul_f32 v[174:175], v[174:175], s[16:17] op_sel_hi:[1,0]
	v_pk_mul_f32 v[176:177], v[176:177], s[16:17] op_sel_hi:[1,0]
	v_pk_mul_f32 v[178:179], v[178:179], s[16:17] op_sel_hi:[1,0]
	v_pk_mul_f32 v[180:181], v[180:181], s[16:17] op_sel_hi:[1,0]
	v_pk_mul_f32 v[182:183], v[182:183], s[16:17] op_sel_hi:[1,0]
	v_pk_mul_f32 v[184:185], v[184:185], s[16:17] op_sel_hi:[1,0]
	v_pk_mul_f32 v[186:187], v[186:187], s[16:17] op_sel_hi:[1,0]
	v_pk_mul_f32 v[188:189], v[188:189], s[16:17] op_sel_hi:[1,0]
	v_pk_mul_f32 v[190:191], v[190:191], s[16:17] op_sel_hi:[1,0]
	v_cvt_pk_fp8_f32 v192, v128, v132
	v_cvt_pk_fp8_f32 v192, v136, v140 op_sel:[0,0,1]
	v_cvt_pk_fp8_f32 v193, v144, v148
	v_cvt_pk_fp8_f32 v193, v152, v156 op_sel:[0,0,1]
	v_cvt_pk_fp8_f32 v194, v160, v164
	v_cvt_pk_fp8_f32 v194, v168, v172 op_sel:[0,0,1]
	v_cvt_pk_fp8_f32 v195, v176, v180
	v_cvt_pk_fp8_f32 v195, v184, v188 op_sel:[0,0,1]
	global_store_dwordx4 v209, v[192:195], s[24:25] sc1
	v_cvt_pk_fp8_f32 v196, v129, v133
	v_cvt_pk_fp8_f32 v196, v137, v141 op_sel:[0,0,1]
	v_cvt_pk_fp8_f32 v197, v145, v149
	v_cvt_pk_fp8_f32 v197, v153, v157 op_sel:[0,0,1]
	v_cvt_pk_fp8_f32 v198, v161, v165
	v_cvt_pk_fp8_f32 v198, v169, v173 op_sel:[0,0,1]
	v_cvt_pk_fp8_f32 v199, v177, v181
	v_cvt_pk_fp8_f32 v199, v185, v189 op_sel:[0,0,1]
	global_store_dwordx4 v209, v[196:199], s[24:25] offset:2048 sc1
	v_cvt_pk_fp8_f32 v200, v130, v134
	v_cvt_pk_fp8_f32 v200, v138, v142 op_sel:[0,0,1]
	v_cvt_pk_fp8_f32 v201, v146, v150
	v_cvt_pk_fp8_f32 v201, v154, v158 op_sel:[0,0,1]
	v_cvt_pk_fp8_f32 v202, v162, v166
	v_cvt_pk_fp8_f32 v202, v170, v174 op_sel:[0,0,1]
	v_cvt_pk_fp8_f32 v203, v178, v182
	v_cvt_pk_fp8_f32 v203, v186, v190 op_sel:[0,0,1]
	global_store_dwordx4 v209, v[200:203], s[26:27] sc1
	v_cvt_pk_fp8_f32 v204, v131, v135
	v_cvt_pk_fp8_f32 v204, v139, v143 op_sel:[0,0,1]
	v_cvt_pk_fp8_f32 v205, v147, v151
	v_cvt_pk_fp8_f32 v205, v155, v159 op_sel:[0,0,1]
	v_cvt_pk_fp8_f32 v206, v163, v167
	v_cvt_pk_fp8_f32 v206, v171, v175 op_sel:[0,0,1]
	v_cvt_pk_fp8_f32 v207, v179, v183
	v_cvt_pk_fp8_f32 v207, v187, v191 op_sel:[0,0,1]
	global_store_dwordx4 v209, v[204:207], s[26:27] offset:2048 sc1
	s_waitcnt vmcnt(8)
	s_add_i32 s1, s20, 60
	s_lshr_b32 s2, s1, 10
	s_and_b32 s4, s1, 0x3ff
	s_lshr_b32 s5, s4, 6
	s_and_b32 s4, s4, 63
	s_lshl_b32 s12, s2, 22
	s_lshl_b32 s13, s4, 16
	s_add_i32 s12, s12, s13
	s_lshl_b32 s13, s5, 7
	s_add_i32 s12, s12, s13
	s_add_u32 s24, s90, s12
	s_addc_u32 s25, s91, 0
	s_add_u32 s24, s24, 0x3b100000
	s_addc_u32 s25, s25, 0
	s_add_u32 s26, s24, 0x1000
	s_addc_u32 s27, s25, 0
	v_pk_mul_f32 v[0:1], v[0:1], s[16:17] op_sel_hi:[1,0]
	v_pk_mul_f32 v[2:3], v[2:3], s[16:17] op_sel_hi:[1,0]
	v_pk_mul_f32 v[4:5], v[4:5], s[16:17] op_sel_hi:[1,0]
	v_pk_mul_f32 v[6:7], v[6:7], s[16:17] op_sel_hi:[1,0]
	v_pk_mul_f32 v[8:9], v[8:9], s[16:17] op_sel_hi:[1,0]
	v_pk_mul_f32 v[10:11], v[10:11], s[16:17] op_sel_hi:[1,0]
	v_pk_mul_f32 v[12:13], v[12:13], s[16:17] op_sel_hi:[1,0]
	v_pk_mul_f32 v[14:15], v[14:15], s[16:17] op_sel_hi:[1,0]
	v_pk_mul_f32 v[16:17], v[16:17], s[16:17] op_sel_hi:[1,0]
	v_pk_mul_f32 v[18:19], v[18:19], s[16:17] op_sel_hi:[1,0]
	v_pk_mul_f32 v[20:21], v[20:21], s[16:17] op_sel_hi:[1,0]
	v_pk_mul_f32 v[22:23], v[22:23], s[16:17] op_sel_hi:[1,0]
	v_pk_mul_f32 v[24:25], v[24:25], s[16:17] op_sel_hi:[1,0]
	v_pk_mul_f32 v[26:27], v[26:27], s[16:17] op_sel_hi:[1,0]
	v_pk_mul_f32 v[28:29], v[28:29], s[16:17] op_sel_hi:[1,0]
	v_pk_mul_f32 v[30:31], v[30:31], s[16:17] op_sel_hi:[1,0]
	v_pk_mul_f32 v[32:33], v[32:33], s[16:17] op_sel_hi:[1,0]
	v_pk_mul_f32 v[34:35], v[34:35], s[16:17] op_sel_hi:[1,0]
	v_pk_mul_f32 v[36:37], v[36:37], s[16:17] op_sel_hi:[1,0]
	v_pk_mul_f32 v[38:39], v[38:39], s[16:17] op_sel_hi:[1,0]
	v_pk_mul_f32 v[40:41], v[40:41], s[16:17] op_sel_hi:[1,0]
	v_pk_mul_f32 v[42:43], v[42:43], s[16:17] op_sel_hi:[1,0]
	v_pk_mul_f32 v[44:45], v[44:45], s[16:17] op_sel_hi:[1,0]
	v_pk_mul_f32 v[46:47], v[46:47], s[16:17] op_sel_hi:[1,0]
	v_pk_mul_f32 v[48:49], v[48:49], s[16:17] op_sel_hi:[1,0]
	v_pk_mul_f32 v[50:51], v[50:51], s[16:17] op_sel_hi:[1,0]
	v_pk_mul_f32 v[52:53], v[52:53], s[16:17] op_sel_hi:[1,0]
	v_pk_mul_f32 v[54:55], v[54:55], s[16:17] op_sel_hi:[1,0]
	v_pk_mul_f32 v[56:57], v[56:57], s[16:17] op_sel_hi:[1,0]
	v_pk_mul_f32 v[58:59], v[58:59], s[16:17] op_sel_hi:[1,0]
	v_pk_mul_f32 v[60:61], v[60:61], s[16:17] op_sel_hi:[1,0]
	v_pk_mul_f32 v[62:63], v[62:63], s[16:17] op_sel_hi:[1,0]
	v_cvt_pk_fp8_f32 v192, v0, v4
	v_cvt_pk_fp8_f32 v192, v8, v12 op_sel:[0,0,1]
	v_cvt_pk_fp8_f32 v193, v16, v20
	v_cvt_pk_fp8_f32 v193, v24, v28 op_sel:[0,0,1]
	v_cvt_pk_fp8_f32 v194, v32, v36
	v_cvt_pk_fp8_f32 v194, v40, v44 op_sel:[0,0,1]
	v_cvt_pk_fp8_f32 v195, v48, v52
	v_cvt_pk_fp8_f32 v195, v56, v60 op_sel:[0,0,1]
	global_store_dwordx4 v209, v[192:195], s[24:25] sc1
	v_cvt_pk_fp8_f32 v196, v1, v5
	v_cvt_pk_fp8_f32 v196, v9, v13 op_sel:[0,0,1]
	v_cvt_pk_fp8_f32 v197, v17, v21
	v_cvt_pk_fp8_f32 v197, v25, v29 op_sel:[0,0,1]
	v_cvt_pk_fp8_f32 v198, v33, v37
	v_cvt_pk_fp8_f32 v198, v41, v45 op_sel:[0,0,1]
	v_cvt_pk_fp8_f32 v199, v49, v53
	v_cvt_pk_fp8_f32 v199, v57, v61 op_sel:[0,0,1]
	global_store_dwordx4 v209, v[196:199], s[24:25] offset:2048 sc1
	v_cvt_pk_fp8_f32 v200, v2, v6
	v_cvt_pk_fp8_f32 v200, v10, v14 op_sel:[0,0,1]
	v_cvt_pk_fp8_f32 v201, v18, v22
	v_cvt_pk_fp8_f32 v201, v26, v30 op_sel:[0,0,1]
	v_cvt_pk_fp8_f32 v202, v34, v38
	v_cvt_pk_fp8_f32 v202, v42, v46 op_sel:[0,0,1]
	v_cvt_pk_fp8_f32 v203, v50, v54
	v_cvt_pk_fp8_f32 v203, v58, v62 op_sel:[0,0,1]
	global_store_dwordx4 v209, v[200:203], s[26:27] sc1
	v_cvt_pk_fp8_f32 v204, v3, v7
	v_cvt_pk_fp8_f32 v204, v11, v15 op_sel:[0,0,1]
	v_cvt_pk_fp8_f32 v205, v19, v23
	v_cvt_pk_fp8_f32 v205, v27, v31 op_sel:[0,0,1]
	v_cvt_pk_fp8_f32 v206, v35, v39
	v_cvt_pk_fp8_f32 v206, v43, v47 op_sel:[0,0,1]
	v_cvt_pk_fp8_f32 v207, v51, v55
	v_cvt_pk_fp8_f32 v207, v59, v63 op_sel:[0,0,1]
	global_store_dwordx4 v209, v[204:207], s[26:27] offset:2048 sc1
	s_waitcnt vmcnt(0)
	v_readlane_b32 s3, v255, 4
